# baseline (speedup 1.0000x reference)
.LBB0_22:
	s_andn2_b64 vcc, exec, s[4:5]
	s_cbranch_vccnz .LBB0_83
	s_movk_i32 s3, 0x200
	v_cmp_gt_u32_e32 vcc, s3, v0
	s_and_saveexec_b64 s[4:5], vcc
	v_mov_b32_e32 v1, 0x10200
	v_lshl_add_u32 v1, v0, 2, v1
	v_mov_b32_e32 v2, 0
	ds_write_b32 v1, v2
	s_or_b64 exec, exec, s[4:5]
	s_load_dwordx4 s[4:7], s[0:1], 0x40
	s_load_dwordx4 s[32:35], s[0:1], 0x70
	s_load_dwordx4 s[36:39], s[0:1], 0x80
	s_mul_i32 s20, s2, 0x1e85
	s_min_i32 s3, s20, 0xf23bb
	s_add_i32 s21, s3, 0x1e85
	v_add_u32_e32 v26, s20, v0
	v_mov_b32_e32 v2, 0
	v_cmp_gt_i32_e32 vcc, s21, v26
	v_mov_b32_e32 v3, v2
	v_mov_b32_e32 v4, v2
	v_mov_b32_e32 v5, v2
	v_mov_b32_e32 v6, v2
	v_mov_b32_e32 v7, v2
	v_mov_b32_e32 v8, v2
	v_mov_b32_e32 v9, v2
	v_mov_b32_e32 v1, -1
	v_mov_b32_e32 v30, -1
	s_waitcnt lgkmcnt(0)
	s_barrier
	s_and_saveexec_b64 s[8:9], vcc
	s_cbranch_execz .LBB0_27
	v_ashrrev_i32_e32 v27, 31, v26
	v_lshlrev_b64 v[10:11], 2, v[26:27]
	v_lshl_add_u64 v[12:13], s[4:5], 0, v[10:11]
	v_lshl_add_u64 v[10:11], s[6:7], 0, v[10:11]
	global_load_dword v2, v[12:13], off
	global_load_dword v30, v[10:11], off

.LBB0_68:
	s_or_b64 exec, exec, s[4:5]
	s_movk_i32 s4, 0xc5
	v_cmp_gt_u32_e32 vcc, s4, v0
	s_and_saveexec_b64 s[4:5], vcc
	s_cbranch_execz .LBB0_70
	v_mov_b32_e32 v1, 0x10a00
	v_lshl_add_u32 v1, v0, 2, v1
	ds_read2st64_b32 v[4:5], v1 offset1:4
	v_lshl_add_u32 v2, v0, 7, s2
	v_ashrrev_i32_e32 v3, 31, v2
	v_lshlrev_b64 v[2:3], 2, v[2:3]
	v_lshl_add_u64 v[6:7], s[34:35], 0, v[2:3]
	v_lshl_add_u64 v[2:3], s[32:33], 0, v[2:3]
	s_waitcnt lgkmcnt(0)
	global_store_dword v[2:3], v4, off
	global_store_dword v[6:7], v5, off
.LBB0_70:
	s_or_b64 exec, exec, s[4:5]
	s_sub_i32 s10, s21, s20
	v_cmp_gt_i32_e32 vcc, s10, v0
	s_waitcnt lgkmcnt(0)
	s_barrier
	s_and_saveexec_b64 s[4:5], vcc
	s_cbranch_execz .LBB0_83
	s_mov_b64 s[4:5], s[36:37]
	s_mov_b64 s[6:7], s[38:39]
	v_sub_u32_e32 v1, s3, v26
	v_add_u32_e32 v1, 0x1e84, v1
	s_movk_i32 s0, 0x3ff
	v_cmp_lt_u32_e32 vcc, s0, v1
	s_mov_b64 s[2:3], -1
	s_and_saveexec_b64 s[0:1], vcc
	s_cbranch_execz .LBB0_80
	v_lshrrev_b32_e32 v6, 10, v1
	v_add_u32_e32 v2, -1, v6
	v_or_b32_e32 v1, 0x400, v0
	v_lshrrev_b32_e32 v3, 1, v2
	s_mov_b32 s11, 0
	v_add_u32_e32 v8, 1, v3
	v_cmp_lt_u32_e32 vcc, 5, v2
	v_mov_b32_e32 v11, 0
	v_lshlrev_b32_e32 v7, 2, v0
	v_mov_b64_e32 v[2:3], v[0:1]
	s_and_saveexec_b64 s[2:3], vcc
	s_cbranch_execz .LBB0_76
	s_add_i32 s12, s20, 0x800
	s_add_i32 s14, s20, 0x1000
	s_add_i32 s16, s20, 0x1800
	v_and_b32_e32 v9, -4, v8
	s_mov_b32 s13, s12
	s_mov_b32 s15, s14
	s_mov_b32 s17, s16
	s_mov_b64 s[8:9], 0
	v_mov_b32_e32 v10, v7
	v_mov_b64_e32 v[2:3], v[0:1]

_Z5k_mlpPKfPKtPKiS4_S4_S4_S2_S2_S2_S0_S0_S0_S0_S0_S0_S0_S4_S4_Pf:
	s_load_dwordx8 s[4:11], s[0:1], 0x48
	s_load_dwordx4 s[12:15], s[0:1], 0x68
	s_load_dwordx2 s[18:19], s[0:1], 0x80
	s_load_dwordx2 s[46:47], s[0:1], 0x88
	s_load_dwordx4 s[48:51], s[0:1], 0x10
	s_load_dwordx2 s[52:53], s[0:1], 0x20
	s_load_dwordx2 s[54:55], s[0:1], 0x8
	s_load_dwordx2 s[56:57], s[0:1], 0x90
	s_load_dwordx2 s[58:59], s[0:1], 0x0
	s_load_dwordx2 s[60:61], s[0:1], 0x30
	v_lshlrev_b32_e32 v6, 2, v0
	s_and_b32 s3, s2, 0xff
	s_mul_i32 s3, s3, 6
	v_mov_b64_e32 v[66:67], 0
	s_ashr_i32 s16, s2, 8
	s_add_i32 s3, s3, s16
	s_cmpk_lt_i32 s2, 0x600
	s_cselect_b32 s2, s3, s2
	v_lshrrev_b32_e32 v1, 6, v0
	v_lshl_or_b32 v3, s2, 1, v1
	v_lshlrev_b32_e32 v2, 5, v3
	v_mov_b32_e32 v7, 32
	s_waitcnt lgkmcnt(0)
	s_load_dword s22, s[18:19], 0x0
	s_load_dword s24, s[18:19], 0x4
	s_load_dword s26, s[18:19], 0x8
	s_load_dword s28, s[18:19], 0xc
	s_load_dword s30, s[18:19], 0x10
	s_load_dword s34, s[18:19], 0x14
	s_load_dword s36, s[18:19], 0x18
	s_load_dword s38, s[18:19], 0x1c
	s_load_dword s33, s[18:19], 0x20
	global_load_dword v8, v6, s[4:5]
	global_load_dword v9, v6, s[6:7]
	global_load_dword v10, v6, s[8:9]
	global_load_dword v11, v6, s[10:11]
	global_load_dword v12, v6, s[12:13]
	global_load_dword v13, v6, s[14:15]
	s_waitcnt lgkmcnt(0)
	s_mov_b64 s[4:5], -1
	s_mul_i32 s2, s22, 39
	s_mul_hi_i32 s2, s2, 0x66666667
	s_lshr_b32 s3, s2, 31
	s_ashr_i32 s23, s2, 9
	s_add_i32 s23, s23, s3
	v_cmp_le_i32_e32 vcc, s23, v3
	s_and_saveexec_b64 s[2:3], vcc
	s_cbranch_execz .LBB2_66
	v_subrev_u32_e32 v3, s23, v3
	v_mov_b32_e32 v7, 32
	v_lshlrev_b32_e32 v2, 5, v3
	v_mov_b64_e32 v[66:67], 1
	s_waitcnt lgkmcnt(0)
	s_mul_i32 s4, s24, 39
	s_mul_hi_i32 s4, s4, 0x66666667
	s_lshr_b32 s5, s4, 31
	s_ashr_i32 s25, s4, 9
	s_add_i32 s25, s25, s5
	v_cmp_le_i32_e32 vcc, s25, v3
	s_mov_b64 s[6:7], -1
	s_and_saveexec_b64 s[4:5], vcc
	s_cbranch_execz .LBB2_65
	v_subrev_u32_e32 v3, s25, v3
	v_mov_b32_e32 v7, 32
	v_lshlrev_b32_e32 v2, 5, v3
	v_mov_b64_e32 v[66:67], 2
	s_waitcnt lgkmcnt(0)
	s_mul_i32 s6, s26, 39
	s_mul_hi_i32 s6, s6, 0x66666667
	s_lshr_b32 s7, s6, 31
	s_ashr_i32 s27, s6, 9
	s_add_i32 s27, s27, s7
	v_cmp_le_i32_e32 vcc, s27, v3
	s_mov_b64 s[8:9], -1
	s_and_saveexec_b64 s[6:7], vcc
	s_cbranch_execz .LBB2_64
	v_subrev_u32_e32 v3, s27, v3
	v_mov_b32_e32 v7, 32
	v_lshlrev_b32_e32 v2, 5, v3
	v_mov_b64_e32 v[66:67], 3
	s_waitcnt lgkmcnt(0)
	s_mul_i32 s8, s28, 39
	s_mul_hi_i32 s8, s8, 0x66666667
	s_lshr_b32 s9, s8, 31
	s_ashr_i32 s29, s8, 9
	s_add_i32 s29, s29, s9
	v_cmp_le_i32_e32 vcc, s29, v3
	s_mov_b64 s[10:11], -1
	s_and_saveexec_b64 s[8:9], vcc
	s_cbranch_execz .LBB2_63
	v_subrev_u32_e32 v3, s29, v3
	v_mov_b32_e32 v7, 32
	v_lshlrev_b32_e32 v2, 5, v3
	v_mov_b64_e32 v[66:67], 4
	s_waitcnt lgkmcnt(0)
	s_mul_i32 s10, s30, 39
	s_mul_hi_i32 s10, s10, 0x66666667
	s_lshr_b32 s11, s10, 31
	s_ashr_i32 s31, s10, 9
	s_add_i32 s31, s31, s11
	v_cmp_le_i32_e32 vcc, s31, v3
	s_mov_b64 s[12:13], -1
	s_and_saveexec_b64 s[10:11], vcc
	s_cbranch_execz .LBB2_62
	v_subrev_u32_e32 v3, s31, v3
	v_mov_b32_e32 v7, 32
	v_lshlrev_b32_e32 v2, 5, v3
	v_mov_b64_e32 v[66:67], 5
	s_waitcnt lgkmcnt(0)
	s_mul_i32 s12, s34, 39
	s_mul_hi_i32 s12, s12, 0x66666667
	s_lshr_b32 s13, s12, 31
	s_ashr_i32 s35, s12, 9
	s_add_i32 s35, s35, s13
	v_cmp_le_i32_e32 vcc, s35, v3
	s_mov_b64 s[14:15], -1
	s_and_saveexec_b64 s[12:13], vcc
	s_cbranch_execz .LBB2_61
	v_subrev_u32_e32 v3, s35, v3
	v_mov_b32_e32 v7, 32
	v_lshlrev_b32_e32 v2, 5, v3
	v_mov_b64_e32 v[66:67], 6
	s_waitcnt lgkmcnt(0)
	s_mul_i32 s14, s36, 39
	s_mul_hi_i32 s14, s14, 0x66666667
	s_lshr_b32 s15, s14, 31
	s_ashr_i32 s37, s14, 9
	s_add_i32 s37, s37, s15
	v_cmp_le_i32_e32 vcc, s37, v3
	s_mov_b64 s[16:17], -1
	s_and_saveexec_b64 s[14:15], vcc
	s_cbranch_execz .LBB2_60
	v_subrev_u32_e32 v3, s37, v3
	v_mov_b32_e32 v7, 32
	v_lshlrev_b32_e32 v2, 5, v3
	v_mov_b64_e32 v[66:67], 7
	s_waitcnt lgkmcnt(0)
	s_mul_i32 s16, s38, 39
	s_mul_hi_i32 s16, s16, 0x66666667
	s_lshr_b32 s17, s16, 31
	s_ashr_i32 s39, s16, 9
	s_add_i32 s39, s39, s17
	v_cmp_le_i32_e32 vcc, s39, v3
	s_mov_b64 s[20:21], -1
	s_and_saveexec_b64 s[16:17], vcc
	s_cbranch_execz .LBB2_59
	v_subrev_u32_e32 v3, s39, v3
	v_mov_b32_e32 v7, 32
	v_lshlrev_b32_e32 v2, 5, v3
	v_mov_b64_e32 v[66:67], 8
	s_waitcnt lgkmcnt(0)
	s_mul_i32 s18, s33, 39
	s_mul_hi_i32 s18, s18, 0x66666667
	s_lshr_b32 s19, s18, 31
	s_ashr_i32 s40, s18, 9
	s_add_i32 s40, s40, s19
	v_cmp_le_i32_e32 vcc, s40, v3
	s_and_saveexec_b64 s[18:19], vcc
	s_cbranch_execz .LBB2_58
	s_lshl_b32 s23, s23, 5
	s_sub_i32 s22, s22, s23
	s_add_i32 s20, s22, 7
	s_ashr_i32 s21, s20, 31
	s_lshr_b32 s21, s21, 29
	s_add_i32 s20, s20, s21
	v_subrev_u32_e32 v3, s40, v3
	s_ashr_i32 s41, s20, 3
	v_cmp_le_i32_e32 vcc, s41, v3
	s_and_saveexec_b64 s[20:21], vcc
	s_xor_b64 s[20:21], exec, s[20:21]
	v_subrev_u32_e32 v3, s41, v3
	s_or_saveexec_b64 s[20:21], s[20:21]
	v_mov_b32_e32 v7, 32
	s_xor_b64 exec, exec, s[20:21]
	v_lshlrev_b32_e32 v4, 3, v3
	v_add_u32_e32 v2, s23, v4
	v_sub_u32_e32 v4, s22, v4
	v_min_i32_e32 v7, 8, v4
	s_or_b64 exec, exec, s[20:21]
	v_mov_b64_e32 v[66:67], 0
	s_mov_b64 s[22:23], -1
	s_and_saveexec_b64 s[20:21], vcc
	s_cbranch_execz .LBB2_57
	s_lshl_b32 s25, s25, 5
	s_sub_i32 s24, s24, s25
	s_add_i32 s22, s24, 7
	s_ashr_i32 s23, s22, 31
	s_lshr_b32 s23, s23, 29
	s_add_i32 s22, s22, s23
	s_ashr_i32 s41, s22, 3
	v_cmp_le_i32_e32 vcc, s41, v3
	s_and_saveexec_b64 s[22:23], vcc
	s_xor_b64 s[22:23], exec, s[22:23]
	v_subrev_u32_e32 v3, s41, v3
	s_andn2_saveexec_b64 s[22:23], s[22:23]
	v_lshlrev_b32_e32 v4, 3, v3
	v_add_u32_e32 v2, s25, v4
	v_sub_u32_e32 v4, s24, v4
	v_min_i32_e32 v7, 8, v4
	s_or_b64 exec, exec, s[22:23]
	v_mov_b64_e32 v[66:67], 1
	s_mov_b64 s[24:25], -1
	s_and_saveexec_b64 s[22:23], vcc
	s_cbranch_execz .LBB2_56
	s_lshl_b32 s27, s27, 5
	s_sub_i32 s26, s26, s27
	s_add_i32 s24, s26, 7
	s_ashr_i32 s25, s24, 31
	s_lshr_b32 s25, s25, 29
	s_add_i32 s24, s24, s25
	s_ashr_i32 s41, s24, 3
	v_cmp_le_i32_e32 vcc, s41, v3
	s_and_saveexec_b64 s[24:25], vcc
	s_xor_b64 s[24:25], exec, s[24:25]
	v_subrev_u32_e32 v3, s41, v3
	s_andn2_saveexec_b64 s[24:25], s[24:25]
	v_lshlrev_b32_e32 v4, 3, v3
	v_add_u32_e32 v2, s27, v4
	v_sub_u32_e32 v4, s26, v4
	v_min_i32_e32 v7, 8, v4
	s_or_b64 exec, exec, s[24:25]
	v_mov_b64_e32 v[66:67], 2
	s_mov_b64 s[26:27], -1
	s_and_saveexec_b64 s[24:25], vcc
	s_cbranch_execz .LBB2_55
	s_lshl_b32 s29, s29, 5
	s_sub_i32 s28, s28, s29
	s_add_i32 s26, s28, 7
	s_ashr_i32 s27, s26, 31
	s_lshr_b32 s27, s27, 29
	s_add_i32 s26, s26, s27
	s_ashr_i32 s41, s26, 3
	v_cmp_le_i32_e32 vcc, s41, v3
	s_and_saveexec_b64 s[26:27], vcc
	s_xor_b64 s[26:27], exec, s[26:27]
	v_subrev_u32_e32 v3, s41, v3
	s_andn2_saveexec_b64 s[26:27], s[26:27]
	v_lshlrev_b32_e32 v4, 3, v3
	v_add_u32_e32 v2, s29, v4
	v_sub_u32_e32 v4, s28, v4
	v_min_i32_e32 v7, 8, v4
	s_or_b64 exec, exec, s[26:27]
	v_mov_b64_e32 v[66:67], 3
	s_mov_b64 s[28:29], -1
	s_and_saveexec_b64 s[26:27], vcc
	s_cbranch_execz .LBB2_54
	s_lshl_b32 s31, s31, 5
	s_sub_i32 s30, s30, s31
	s_add_i32 s28, s30, 7
	s_ashr_i32 s29, s28, 31
	s_lshr_b32 s29, s29, 29
	s_add_i32 s28, s28, s29
	s_ashr_i32 s41, s28, 3
	v_cmp_le_i32_e32 vcc, s41, v3
	s_and_saveexec_b64 s[28:29], vcc
	s_xor_b64 s[28:29], exec, s[28:29]
	v_subrev_u32_e32 v3, s41, v3
	s_andn2_saveexec_b64 s[28:29], s[28:29]
	v_lshlrev_b32_e32 v4, 3, v3
	v_add_u32_e32 v2, s31, v4
	v_sub_u32_e32 v4, s30, v4
	v_min_i32_e32 v7, 8, v4
	s_or_b64 exec, exec, s[28:29]
	v_mov_b64_e32 v[66:67], 4
	s_mov_b64 s[30:31], -1
	s_and_saveexec_b64 s[28:29], vcc
	s_cbranch_execz .LBB2_53
	s_lshl_b32 s35, s35, 5
	s_sub_i32 s34, s34, s35
	s_add_i32 s30, s34, 7
	s_ashr_i32 s31, s30, 31
	s_lshr_b32 s31, s31, 29
	s_add_i32 s30, s30, s31
	s_ashr_i32 s41, s30, 3
	v_cmp_le_i32_e32 vcc, s41, v3
	s_and_saveexec_b64 s[30:31], vcc
	s_xor_b64 s[30:31], exec, s[30:31]
	v_subrev_u32_e32 v3, s41, v3
	s_andn2_saveexec_b64 s[30:31], s[30:31]
	v_lshlrev_b32_e32 v4, 3, v3
	v_add_u32_e32 v2, s35, v4
	v_sub_u32_e32 v4, s34, v4
	v_min_i32_e32 v7, 8, v4
	s_or_b64 exec, exec, s[30:31]
	v_mov_b64_e32 v[66:67], 5
	s_mov_b64 s[34:35], -1
	s_and_saveexec_b64 s[30:31], vcc
	s_cbranch_execz .LBB2_52
	s_lshl_b32 s37, s37, 5
	s_sub_i32 s36, s36, s37
	s_add_i32 s34, s36, 7
	s_ashr_i32 s35, s34, 31
	s_lshr_b32 s35, s35, 29
	s_add_i32 s34, s34, s35
	s_ashr_i32 s41, s34, 3
	v_cmp_le_i32_e32 vcc, s41, v3
	s_and_saveexec_b64 s[34:35], vcc
	s_xor_b64 s[34:35], exec, s[34:35]
	v_subrev_u32_e32 v3, s41, v3
	s_andn2_saveexec_b64 s[34:35], s[34:35]
	v_lshlrev_b32_e32 v4, 3, v3
	v_add_u32_e32 v2, s37, v4
	v_sub_u32_e32 v4, s36, v4
	v_min_i32_e32 v7, 8, v4
	s_or_b64 exec, exec, s[34:35]
	v_mov_b64_e32 v[66:67], 6
	s_mov_b64 s[36:37], -1
	s_and_saveexec_b64 s[34:35], vcc
	s_cbranch_execz .LBB2_51
	s_lshl_b32 s39, s39, 5
	s_sub_i32 s38, s38, s39
	s_add_i32 s36, s38, 7
	s_ashr_i32 s37, s36, 31
	s_lshr_b32 s37, s37, 29
	s_add_i32 s36, s36, s37
	s_ashr_i32 s41, s36, 3
	v_cmp_le_i32_e32 vcc, s41, v3
	s_and_saveexec_b64 s[36:37], vcc
	s_xor_b64 s[36:37], exec, s[36:37]
	v_subrev_u32_e32 v3, s41, v3
	s_andn2_saveexec_b64 s[36:37], s[36:37]
	v_lshlrev_b32_e32 v4, 3, v3
	v_add_u32_e32 v2, s39, v4
	v_sub_u32_e32 v4, s38, v4
	v_min_i32_e32 v7, 8, v4
	s_or_b64 exec, exec, s[36:37]
	v_mov_b64_e32 v[66:67], 7
	s_mov_b64 s[38:39], -1
	s_and_saveexec_b64 s[36:37], vcc
	s_cbranch_execz .LBB2_50
	s_lshl_b32 s38, s40, 5
	s_sub_i32 s33, s33, s38
	s_add_i32 s39, s33, 7
	s_ashr_i32 s40, s39, 31
	s_lshr_b32 s40, s40, 29
	s_add_i32 s39, s39, s40
	v_lshlrev_b32_e32 v4, 3, v3
	s_ashr_i32 s39, s39, 3
	v_add_u32_e32 v5, s38, v4
	v_sub_u32_e32 v4, s33, v4
	v_min_i32_e32 v4, 8, v4
	v_cmp_gt_i32_e32 vcc, s39, v3
	s_orn2_b64 s[38:39], vcc, exec
	s_nop 0
	v_cndmask_b32_e32 v7, v7, v4, vcc
	v_cndmask_b32_e32 v2, v2, v5, vcc
	v_cndmask_b32_e64 v66, 9, 8, vcc

.LBB2_66:
	s_or_b64 exec, exec, s[2:3]
	s_waitcnt vmcnt(0)
	ds_write_b32 v6, v8 offset:17408
	ds_write_b32 v6, v9 offset:17920
	ds_write_b32 v6, v10 offset:18432
	ds_write_b32 v6, v11 offset:18944
	ds_write_b32 v6, v12 offset:19456
	ds_write_b32 v6, v13 offset:19968
	s_waitcnt lgkmcnt(0)
	s_barrier
	s_and_saveexec_b64 s[2:3], s[4:5]
	s_cbranch_execz .LBB2_134
	v_and_b32_e32 v146, 63, v0
	v_cmp_lt_i32_e32 vcc, v146, v7
	v_mov_b32_e32 v4, -1
	s_and_saveexec_b64 s[2:3], vcc
	s_cbranch_execz .LBB2_69
	s_mov_b64 s[4:5], s[46:47]
	s_mov_b32 s6, 0x61a80
	v_ashrrev_i32_e32 v3, 31, v2
	v_lshlrev_b32_e32 v4, 2, v146
	v_mov_b32_e32 v5, 0
	s_waitcnt lgkmcnt(0)
	v_mov_b64_e32 v[8:9], s[4:5]
	v_mad_u64_u32 v[8:9], s[4:5], v66, s6, v[8:9]
	v_lshl_add_u64 v[2:3], v[2:3], 2, v[8:9]
	v_lshl_add_u64 v[2:3], v[2:3], 0, v[4:5]
	global_load_dword v4, v[2:3], off

.LBB2_71:
	s_or_b64 exec, exec, s[2:3]
	s_waitcnt vmcnt(0)
	v_cmp_lt_i32_e32 vcc, -1, v4
	v_mov_b32_e32 v67, 0
	v_mov_b32_e32 v75, 1
	v_mov_b32_e32 v69, 0
	s_and_saveexec_b64 s[2:3], vcc
	s_cbranch_execz .LBB2_73
	s_mov_b64 s[4:5], s[48:49]
	s_mov_b64 s[6:7], s[50:51]
	s_mov_b64 s[8:9], s[52:53]
	v_mov_b32_e32 v5, 0
	v_lshlrev_b64 v[2:3], 2, v[4:5]
	s_waitcnt lgkmcnt(0)
	v_lshl_add_u64 v[4:5], s[4:5], 0, v[2:3]
	v_lshl_add_u64 v[8:9], s[6:7], 0, v[2:3]
	v_lshl_add_u64 v[2:3], s[8:9], 0, v[2:3]
	global_load_dword v69, v[4:5], off
	global_load_dword v67, v[8:9], off
	global_load_dword v75, v[2:3], off

.LBB2_90:
	s_or_b64 exec, exec, s[4:5]
	s_load_dwordx2 s[34:35], s[0:1], 0x78
	s_load_dwordx2 s[36:37], s[0:1], 0x40
	v_ashrrev_i32_e32 v78, 2, v7
	v_and_b32_e32 v147, 48, v0
	v_cmp_lt_i32_e32 vcc, 0, v78
	s_and_saveexec_b64 s[40:41], vcc
	s_cbranch_execz .LBB2_101
	s_mov_b64 s[2:3], s[54:55]
	v_lshlrev_b32_e32 v2, 3, v131
	v_mov_b32_e32 v3, 0
	v_lshlrev_b32_e32 v2, 1, v2
	v_lshlrev_b32_e32 v79, 2, v84
	s_waitcnt lgkmcnt(0)
	v_lshl_add_u64 v[70:71], s[2:3], 0, v[2:3]
	v_or_b32_e32 v2, v147, v84
	v_lshlrev_b32_e32 v86, 2, v2
	v_lshlrev_b32_e32 v2, 2, v83
	v_and_b32_e32 v3, 0xc0, v6
	s_movk_i32 s2, 0x100
	v_or_b32_e32 v80, 64, v79
	v_or_b32_e32 v81, 0x80, v79
	v_or_b32_e32 v85, 0xc0, v79
	v_or_b32_e32 v87, 4, v86
	v_or_b32_e32 v88, 8, v86
	v_or_b32_e32 v89, 12, v86
	v_or_b32_e32 v90, 16, v86
	v_or_b32_e32 v91, 20, v86
	v_or_b32_e32 v92, 24, v86
	v_or_b32_e32 v93, 28, v86
	v_or_b32_e32 v94, 32, v86
	v_or_b32_e32 v95, 36, v86
	v_or_b32_e32 v96, 40, v86
	v_or_b32_e32 v97, 44, v86
	v_or_b32_e32 v98, 48, v86
	v_or_b32_e32 v99, 52, v86
	v_or_b32_e32 v100, 56, v86
	v_or_b32_e32 v101, 60, v86
	v_and_or_b32 v102, v2, s2, v3
	s_mov_b32 s33, 0
	s_mov_b64 s[42:43], 0
	s_movk_i32 s44, 0x110
	s_waitcnt vmcnt(0)
	v_mov_b32_e32 v105, v30
	v_mov_b32_e32 v103, v76
	v_mov_b32_e32 v104, v77
	s_branch .LBB2_93

.LBB2_101:
	s_or_b64 exec, exec, s[40:41]
	s_mov_b64 s[2:3], s[56:57]
	s_mov_b64 s[4:5], s[58:59]
	s_mov_b64 s[6:7], s[60:61]
	v_lshlrev_b32_e32 v132, 15, v66
	v_mov_b32_e32 v133, 0
	s_waitcnt lgkmcnt(0)
	v_lshl_add_u64 v[26:27], s[6:7], 0, v[132:133]
	v_lshlrev_b32_e32 v132, 4, v146
	v_lshl_add_u64 v[66:67], v[26:27], 0, v[132:133]
	s_movk_i32 s9, 0x1000
	v_add_co_u32_e32 v68, vcc, s9, v66
	s_movk_i32 s11, 0x2000
	s_nop 0
	v_addc_co_u32_e32 v69, vcc, 0, v67, vcc
	v_add_co_u32_e32 v70, vcc, s11, v66
	global_load_dwordx4 v[86:89], v[66:67], off
	s_nop 0
	v_addc_co_u32_e32 v71, vcc, 0, v67, vcc
	global_load_dwordx4 v[90:93], v[70:71], off offset:-4096
	s_movk_i32 s12, 0x3000
	v_add_co_u32_e32 v72, vcc, s12, v66
	s_movk_i32 s8, 0x4000
	s_nop 0
	v_addc_co_u32_e32 v73, vcc, 0, v67, vcc
	v_add_co_u32_e32 v74, vcc, s8, v66
	global_load_dwordx4 v[94:97], v[70:71], off
	s_waitcnt vmcnt(4)
	v_addc_co_u32_e32 v75, vcc, 0, v67, vcc
	global_load_dwordx4 v[98:101], v[74:75], off offset:-4096
	s_movk_i32 s10, 0x5000
	v_add_co_u32_e32 v76, vcc, s10, v66
	s_movk_i32 s7, 0x6000
	s_nop 0
	v_addc_co_u32_e32 v77, vcc, 0, v67, vcc
	v_add_co_u32_e32 v78, vcc, s7, v66
	global_load_dwordx4 v[102:105], v[74:75], off
	s_nop 0
	v_addc_co_u32_e32 v79, vcc, 0, v67, vcc
	global_load_dwordx4 v[110:113], v[78:79], off
	global_load_dwordx4 v[106:109], v[78:79], off offset:-4096
	s_movk_i32 s6, 0x7000
	v_add_co_u32_e32 v80, vcc, s6, v66
	s_movk_i32 s0, 0x110
	s_nop 0
	v_addc_co_u32_e32 v81, vcc, 0, v67, vcc
	global_load_dwordx4 v[114:117], v[80:81], off
	global_load_dwordx4 v[58:61], v[66:67], off offset:1024
	global_load_dwordx4 v[62:65], v[68:69], off offset:1024
	global_load_dwordx4 v[54:57], v[70:71], off offset:1024
	global_load_dwordx4 v[50:53], v[72:73], off offset:1024
	global_load_dwordx4 v[46:49], v[74:75], off offset:1024
	global_load_dwordx4 v[42:45], v[76:77], off offset:1024
	global_load_dwordx4 v[34:37], v[78:79], off offset:1024
	global_load_dwordx4 v[26:29], v[80:81], off offset:1024
	v_mad_u32_u24 v85, v131, s0, v130
	v_add_u32_e32 v151, v85, v147
	ds_read_b128 v[38:41], v147 offset:17408
	s_waitcnt vmcnt(16)
	ds_read_b128 v[30:33], v147 offset:17472
	ds_read_b128 v[118:121], v151
	ds_read_b128 v[122:125], v151 offset:4352
	ds_read_b128 v[164:167], v151 offset:4416
	s_waitcnt vmcnt(15) lgkmcnt(2)
	v_mfma_f32_16x16x32_f16 v[126:129], v[86:89], v[118:121], v[38:41]
	s_waitcnt lgkmcnt(1)
	v_mfma_f32_16x16x32_f16 v[86:89], v[86:89], v[122:125], v[38:41]
	s_waitcnt vmcnt(14)
	v_mfma_f32_16x16x32_f16 v[134:137], v[90:93], v[118:121], v[30:33]
	v_mfma_f32_16x16x32_f16 v[90:93], v[90:93], v[122:125], v[30:33]
	global_load_dwordx4 v[38:41], v[66:67], off offset:2048
	s_nop 1
	global_load_dwordx4 v[30:33], v[68:69], off offset:2048
	ds_read_b128 v[22:25], v147 offset:17536
	ds_read_b128 v[18:21], v147 offset:17600
	s_waitcnt vmcnt(15) lgkmcnt(1)
	v_mfma_f32_16x16x32_f16 v[138:141], v[94:97], v[118:121], v[22:25]
	v_mfma_f32_16x16x32_f16 v[94:97], v[94:97], v[122:125], v[22:25]
	s_waitcnt vmcnt(14) lgkmcnt(0)
	v_mfma_f32_16x16x32_f16 v[142:145], v[98:101], v[118:121], v[18:21]
	v_mfma_f32_16x16x32_f16 v[98:101], v[98:101], v[122:125], v[18:21]
	global_load_dwordx4 v[22:25], v[70:71], off offset:2048
	s_nop 1
	global_load_dwordx4 v[18:21], v[72:73], off offset:2048
	ds_read_b128 v[6:9], v147 offset:17792
	s_waitcnt vmcnt(14) lgkmcnt(0)
	v_mfma_f32_16x16x32_f16 v[160:163], v[110:113], v[118:121], v[6:9]
	v_mfma_f32_16x16x32_f16 v[110:113], v[110:113], v[122:125], v[6:9]
	s_nop 2
	global_load_dwordx4 v[6:9], v[78:79], off offset:2048
	ds_read_b128 v[10:13], v147 offset:17728
	s_waitcnt vmcnt(14) lgkmcnt(0)
	v_mfma_f32_16x16x32_f16 v[156:159], v[106:109], v[118:121], v[10:13]
	v_mfma_f32_16x16x32_f16 v[106:109], v[106:109], v[122:125], v[10:13]
	s_nop 2
	global_load_dwordx4 v[10:13], v[76:77], off offset:2048
	ds_read_b128 v[14:17], v147 offset:17664
	s_waitcnt lgkmcnt(0)
	v_mfma_f32_16x16x32_f16 v[152:155], v[102:105], v[118:121], v[14:17]
	ds_read_b128 v[2:5], v147 offset:17856
	s_waitcnt vmcnt(14) lgkmcnt(0)
	v_mfma_f32_16x16x32_f16 v[118:121], v[114:117], v[118:121], v[2:5]
	v_mfma_f32_16x16x32_f16 v[114:117], v[114:117], v[122:125], v[2:5]
	s_nop 2
	global_load_dwordx4 v[2:5], v[80:81], off offset:2048
	v_mfma_f32_16x16x32_f16 v[102:105], v[102:105], v[122:125], v[14:17]
	ds_read_b128 v[122:125], v151 offset:64
	s_nop 1
	global_load_dwordx4 v[14:17], v[74:75], off offset:2048
	s_waitcnt vmcnt(15) lgkmcnt(0)
	v_mfma_f32_16x16x32_f16 v[126:129], v[58:61], v[122:125], v[126:129]
	v_mfma_f32_16x16x32_f16 v[58:61], v[58:61], v[164:167], v[86:89]
	s_waitcnt vmcnt(14)
	v_mfma_f32_16x16x32_f16 v[86:89], v[62:65], v[122:125], v[134:137]
	v_mfma_f32_16x16x32_f16 v[62:65], v[62:65], v[164:167], v[90:93]
	s_nop 1
	global_load_dwordx4 v[134:137], v[70:71], off offset:3072
	s_nop 0
	global_load_dwordx4 v[70:73], v[72:73], off offset:3072
	s_waitcnt vmcnt(15)
	v_mfma_f32_16x16x32_f16 v[90:93], v[54:57], v[122:125], v[138:141]
	v_mfma_f32_16x16x32_f16 v[54:57], v[54:57], v[164:167], v[94:97]
	s_nop 1
	global_load_dwordx4 v[138:141], v[74:75], off offset:3072
	s_nop 0
	global_load_dwordx4 v[74:77], v[76:77], off offset:3072
	s_waitcnt vmcnt(16)
	v_mfma_f32_16x16x32_f16 v[94:97], v[50:53], v[122:125], v[142:145]
	v_mfma_f32_16x16x32_f16 v[50:53], v[50:53], v[164:167], v[98:101]
	s_nop 1
	global_load_dwordx4 v[142:145], v[78:79], off offset:3072
	s_nop 0
	global_load_dwordx4 v[78:81], v[80:81], off offset:3072
	s_waitcnt vmcnt(17)
	v_mfma_f32_16x16x32_f16 v[98:101], v[46:49], v[122:125], v[152:155]
	v_mfma_f32_16x16x32_f16 v[46:49], v[46:49], v[164:167], v[102:105]
	s_waitcnt vmcnt(16)
	v_mfma_f32_16x16x32_f16 v[102:105], v[42:45], v[122:125], v[156:159]
	v_mfma_f32_16x16x32_f16 v[42:45], v[42:45], v[164:167], v[106:109]
	s_waitcnt vmcnt(15)
	v_mfma_f32_16x16x32_f16 v[106:109], v[34:37], v[122:125], v[160:163]
	v_mfma_f32_16x16x32_f16 v[34:37], v[34:37], v[164:167], v[110:113]
	s_waitcnt vmcnt(14)
	v_mfma_f32_16x16x32_f16 v[110:113], v[26:29], v[122:125], v[118:121]
	ds_read_b128 v[122:125], v151 offset:4480
	v_mfma_f32_16x16x32_f16 v[26:29], v[26:29], v[164:167], v[114:117]
	s_nop 0
	ds_read_b128 v[118:121], v151 offset:128
	s_nop 0
	global_load_dwordx4 v[114:117], v[66:67], off offset:3072
	s_nop 0
	global_load_dwordx4 v[66:69], v[68:69], off offset:3072
	s_waitcnt vmcnt(15) lgkmcnt(0)
	v_mfma_f32_16x16x32_f16 v[126:129], v[38:41], v[118:121], v[126:129]
	v_mfma_f32_16x16x32_f16 v[38:41], v[38:41], v[122:125], v[58:61]
	s_waitcnt vmcnt(14)
	v_mfma_f32_16x16x32_f16 v[58:61], v[30:33], v[118:121], v[86:89]
	s_waitcnt vmcnt(13)
	v_mfma_f32_16x16x32_f16 v[86:89], v[22:25], v[118:121], v[90:93]
	v_mfma_f32_16x16x32_f16 v[22:25], v[22:25], v[122:125], v[54:57]
	s_nop 1
	ds_read_b128 v[90:93], v151 offset:192
	s_waitcnt vmcnt(12)
	v_mfma_f32_16x16x32_f16 v[54:57], v[18:21], v[118:121], v[94:97]
	s_nop 2
	ds_read_b128 v[94:97], v151 offset:4544
	v_mfma_f32_16x16x32_f16 v[62:65], v[30:33], v[122:125], v[62:65]
	v_mfma_f32_16x16x32_f16 v[18:21], v[18:21], v[122:125], v[50:53]
	s_waitcnt vmcnt(8)
	v_mfma_f32_16x16x32_f16 v[50:53], v[14:17], v[118:121], v[98:101]
	v_mfma_f32_16x16x32_f16 v[14:17], v[14:17], v[122:125], v[46:49]
	v_mfma_f32_16x16x32_f16 v[46:49], v[10:13], v[118:121], v[102:105]
	v_mfma_f32_16x16x32_f16 v[10:13], v[10:13], v[122:125], v[42:45]
	v_mfma_f32_16x16x32_f16 v[42:45], v[6:9], v[118:121], v[106:109]
	v_mfma_f32_16x16x32_f16 v[6:9], v[6:9], v[122:125], v[34:37]
	v_mfma_f32_16x16x32_f16 v[34:37], v[2:5], v[118:121], v[110:113]
	v_mfma_f32_16x16x32_f16 v[2:5], v[2:5], v[122:125], v[26:29]
	s_waitcnt vmcnt(1) lgkmcnt(0)
	v_mfma_f32_16x16x32_f16 v[30:33], v[114:117], v[94:97], v[38:41]
	s_waitcnt vmcnt(0)
	v_mfma_f32_16x16x32_f16 v[26:29], v[66:69], v[94:97], v[62:65]
	v_mfma_f32_16x16x32_f16 v[22:25], v[134:137], v[94:97], v[22:25]
	v_mfma_f32_16x16x32_f16 v[18:21], v[70:73], v[94:97], v[18:21]
	v_mfma_f32_16x16x32_f16 v[14:17], v[138:141], v[94:97], v[14:17]
	v_mfma_f32_16x16x32_f16 v[10:13], v[74:77], v[94:97], v[10:13]
	v_mfma_f32_16x16x32_f16 v[6:9], v[142:145], v[94:97], v[6:9]
	v_mfma_f32_16x16x32_f16 v[2:5], v[78:81], v[94:97], v[2:5]
	v_mfma_f32_16x16x32_f16 v[126:129], v[114:117], v[90:93], v[126:129]
	v_mfma_f32_16x16x32_f16 v[122:125], v[66:69], v[90:93], v[58:61]
	v_mfma_f32_16x16x32_f16 v[118:121], v[134:137], v[90:93], v[86:89]
	v_mfma_f32_16x16x32_f16 v[114:117], v[70:73], v[90:93], v[54:57]
	v_mfma_f32_16x16x32_f16 v[106:109], v[138:141], v[90:93], v[50:53]
	v_mfma_f32_16x16x32_f16 v[110:113], v[74:77], v[90:93], v[46:49]
	v_mfma_f32_16x16x32_f16 v[102:105], v[142:145], v[90:93], v[42:45]
	v_mfma_f32_16x16x32_f16 v[98:101], v[78:81], v[90:93], v[34:37]
	s_nop 2
	v_xor_b32_e32 v34, 16, v83
	v_add_u32_e32 v35, 64, v84
	v_cmp_lt_i32_e32 vcc, v34, v35
	v_mov_b32_e32 v36, v127
	v_mov_b32_e32 v37, v123
	v_cndmask_b32_e32 v34, v83, v34, vcc
	v_lshlrev_b32_e32 v149, 2, v34
	v_xor_b32_e32 v34, 32, v83
	v_cmp_lt_i32_e32 vcc, v34, v35
	v_mov_b32_e32 v35, v122
	v_mov_b32_e32 v38, v129
	v_cndmask_b32_e32 v34, v83, v34, vcc
	v_lshlrev_b32_e32 v148, 2, v34
	v_mov_b32_e32 v34, v126
	v_pk_add_f32 v[34:35], v[34:35], v[36:37]
	v_mov_b32_e32 v36, v128
	v_mov_b32_e32 v37, v124
	v_mov_b32_e32 v39, v125
	v_pk_add_f32 v[36:37], v[36:37], v[38:39]
	v_mov_b32_e32 v38, v118
	v_pk_add_f32 v[34:35], v[34:35], v[36:37]
	v_mov_b32_e32 v36, v119
	v_mov_b32_e32 v37, v120
	v_mov_b32_e32 v39, v121
	v_pk_add_f32 v[36:37], v[36:37], v[38:39]
	v_add_f32_e32 v34, 0, v34
	v_pk_add_f32 v[36:37], v[36:37], v[36:37] op_sel:[0,1] op_sel_hi:[1,0]
	v_add_f32_e32 v34, v34, v35
	v_add_f32_e32 v38, v114, v115
	v_add_f32_e32 v40, v116, v117
	v_mov_b32_e32 v35, v106
	v_mov_b32_e32 v37, v107
	v_mov_b32_e32 v39, v108
	v_mov_b32_e32 v41, v109
	v_pk_add_f32 v[34:35], v[34:35], v[36:37]
	v_pk_add_f32 v[36:37], v[38:39], v[40:41]
	v_mov_b32_e32 v38, v110
	v_pk_add_f32 v[34:35], v[34:35], v[36:37]
	v_mov_b32_e32 v36, v111
	v_mov_b32_e32 v37, v112
	v_mov_b32_e32 v39, v113
	v_pk_add_f32 v[36:37], v[36:37], v[38:39]
	v_pk_add_f32 v[34:35], v[34:35], v[34:35] op_sel:[0,1] op_sel_hi:[1,0]
	v_pk_add_f32 v[36:37], v[36:37], v[36:37] op_sel:[0,1] op_sel_hi:[1,0]
	v_add_f32_e32 v38, v102, v103
	v_add_f32_e32 v40, v104, v105
	v_mov_b32_e32 v35, v98
	v_mov_b32_e32 v37, v99
	v_mov_b32_e32 v39, v100
	v_mov_b32_e32 v41, v101
	v_pk_add_f32 v[34:35], v[34:35], v[36:37]
	v_pk_add_f32 v[36:37], v[38:39], v[40:41]
	v_mov_b32_e32 v38, v31
	v_pk_add_f32 v[34:35], v[34:35], v[36:37]
	v_mov_b32_e32 v36, v30
	v_mov_b32_e32 v37, v26
	v_mov_b32_e32 v39, v27
	v_pk_add_f32 v[36:37], v[36:37], v[38:39]
	v_mov_b32_e32 v38, v32
	v_mov_b32_e32 v39, v28
	v_mov_b32_e32 v40, v33
	v_mov_b32_e32 v41, v29
	v_pk_add_f32 v[38:39], v[38:39], v[40:41]
	v_mov_b32_e32 v40, v22
	v_pk_add_f32 v[36:37], v[36:37], v[38:39]
	v_mov_b32_e32 v38, v23
	v_mov_b32_e32 v39, v24
	v_mov_b32_e32 v41, v25
	v_pk_add_f32 v[38:39], v[38:39], v[40:41]
	v_add_f32_e32 v36, 0, v36
	v_pk_add_f32 v[38:39], v[38:39], v[38:39] op_sel:[0,1] op_sel_hi:[1,0]
	v_add_f32_e32 v36, v36, v37
	v_add_f32_e32 v40, v18, v19
	v_add_f32_e32 v42, v20, v21
	v_mov_b32_e32 v37, v14
	v_mov_b32_e32 v39, v15
	v_mov_b32_e32 v41, v16
	v_mov_b32_e32 v43, v17
	v_pk_add_f32 v[36:37], v[36:37], v[38:39]
	v_pk_add_f32 v[38:39], v[40:41], v[42:43]
	v_mov_b32_e32 v40, v10
	v_pk_add_f32 v[36:37], v[36:37], v[38:39]
	v_mov_b32_e32 v38, v11
	v_mov_b32_e32 v39, v12
	v_mov_b32_e32 v41, v13
	v_pk_add_f32 v[38:39], v[38:39], v[40:41]
	v_pk_add_f32 v[36:37], v[36:37], v[36:37] op_sel:[0,1] op_sel_hi:[1,0]
	v_pk_add_f32 v[38:39], v[38:39], v[38:39] op_sel:[0,1] op_sel_hi:[1,0]
	v_add_f32_e32 v40, v6, v7
	v_add_f32_e32 v42, v8, v9
	v_mov_b32_e32 v37, v2
	v_mov_b32_e32 v39, v3
	v_mov_b32_e32 v41, v4
	v_mov_b32_e32 v43, v5
	v_pk_add_f32 v[36:37], v[36:37], v[38:39]
	v_pk_add_f32 v[38:39], v[40:41], v[42:43]
	s_brev_b32 s0, 60
	v_pk_add_f32 v[36:37], v[36:37], v[38:39]
	v_mov_b32_e32 v39, v34
	v_mov_b32_e32 v38, v36
	v_mov_b32_e32 v34, v37
	v_pk_add_f32 v[34:35], v[38:39], v[34:35]
	ds_bpermute_b32 v37, v149, v35
	ds_bpermute_b32 v36, v149, v34
	v_mov_b32_e32 v165, v126
	v_mov_b32_e32 v164, v30
	v_lshlrev_b32_e32 v150, 4, v82
	ds_read_b128 v[38:41], v150 offset:18880
	s_waitcnt lgkmcnt(1)
	v_pk_add_f32 v[134:135], v[34:35], v[36:37]
	ds_bpermute_b32 v137, v148, v135
	ds_bpermute_b32 v136, v148, v134
	ds_read_b128 v[34:37], v150 offset:18368
	ds_read_b128 v[42:45], v150 offset:18304
	ds_read_b128 v[46:49], v150 offset:18816
	ds_read_b128 v[90:93], v150 offset:17920
	s_waitcnt lgkmcnt(4)
	v_pk_add_f32 v[144:145], v[134:135], v[136:137]
	ds_read_b128 v[94:97], v150 offset:18432
	v_pk_mul_f32 v[134:135], v[144:145], s[0:1] op_sel_hi:[1,0]
	v_pk_fma_f32 v[164:165], v[144:145], s[0:1], v[164:165] op_sel_hi:[1,0,1] neg_lo:[1,0,0] neg_hi:[1,0,0]
	v_sub_f32_e32 v163, v126, v135
	v_mov_b32_e32 v126, v31
	v_sub_f32_e32 v162, v127, v135
	v_pk_fma_f32 v[126:127], v[144:145], s[0:1], v[126:127] op_sel_hi:[1,0,1] neg_lo:[1,0,0] neg_hi:[1,0,0]
	v_sub_f32_e32 v161, v128, v135
	v_pk_mul_f32 v[126:127], v[126:127], v[126:127]
	v_sub_f32_e32 v159, v122, v135
	v_pk_fma_f32 v[126:127], v[164:165], v[164:165], v[126:127]
	v_mov_b32_e32 v164, v32
	v_mov_b32_e32 v165, v128
	v_pk_fma_f32 v[164:165], v[144:145], s[0:1], v[164:165] op_sel_hi:[1,0,1] neg_lo:[1,0,0] neg_hi:[1,0,0]
	v_mov_b32_e32 v128, v33
	v_pk_fma_f32 v[126:127], v[164:165], v[164:165], v[126:127]
	v_pk_fma_f32 v[164:165], v[144:145], s[0:1], v[128:129] op_sel_hi:[1,0,1] neg_lo:[1,0,0] neg_hi:[1,0,0]
	v_sub_f32_e32 v158, v123, v135
	v_pk_fma_f32 v[126:127], v[164:165], v[164:165], v[126:127]
	v_mov_b32_e32 v164, v26
	v_mov_b32_e32 v165, v122
	v_pk_fma_f32 v[164:165], v[144:145], s[0:1], v[164:165] op_sel_hi:[1,0,1] neg_lo:[1,0,0] neg_hi:[1,0,0]
	v_mov_b32_e32 v122, v27
	v_pk_fma_f32 v[126:127], v[164:165], v[164:165], v[126:127]
	v_pk_fma_f32 v[122:123], v[144:145], s[0:1], v[122:123] op_sel_hi:[1,0,1] neg_lo:[1,0,0] neg_hi:[1,0,0]
	v_sub_f32_e32 v156, v124, v135
	v_pk_fma_f32 v[122:123], v[122:123], v[122:123], v[126:127]
	v_mov_b32_e32 v126, v28
	v_mov_b32_e32 v127, v124
	v_pk_fma_f32 v[126:127], v[144:145], s[0:1], v[126:127] op_sel_hi:[1,0,1] neg_lo:[1,0,0] neg_hi:[1,0,0]
	v_mov_b32_e32 v124, v29
	v_pk_fma_f32 v[122:123], v[126:127], v[126:127], v[122:123]
	v_pk_fma_f32 v[164:165], v[144:145], s[0:1], v[124:125] op_sel_hi:[1,0,1] neg_lo:[1,0,0] neg_hi:[1,0,0]
	v_sub_f32_e32 v153, v118, v135
	v_pk_fma_f32 v[122:123], v[164:165], v[164:165], v[122:123]
	v_mov_b32_e32 v164, v22
	v_mov_b32_e32 v165, v118
	v_pk_fma_f32 v[164:165], v[144:145], s[0:1], v[164:165] op_sel_hi:[1,0,1] neg_lo:[1,0,0] neg_hi:[1,0,0]
	v_mov_b32_e32 v118, v23
	v_sub_f32_e32 v157, v119, v135
	v_pk_fma_f32 v[122:123], v[164:165], v[164:165], v[122:123]
	v_pk_fma_f32 v[118:119], v[144:145], s[0:1], v[118:119] op_sel_hi:[1,0,1] neg_lo:[1,0,0] neg_hi:[1,0,0]
	v_sub_f32_e32 v155, v120, v135
	v_pk_fma_f32 v[118:119], v[118:119], v[118:119], v[122:123]
	v_mov_b32_e32 v122, v24
	v_mov_b32_e32 v123, v120
	v_pk_fma_f32 v[122:123], v[144:145], s[0:1], v[122:123] op_sel_hi:[1,0,1] neg_lo:[1,0,0] neg_hi:[1,0,0]
	v_mov_b32_e32 v120, v25
	v_sub_f32_e32 v160, v129, v135
	v_sub_f32_e32 v129, v121, v135
	v_pk_fma_f32 v[164:165], v[122:123], v[122:123], v[118:119]
	v_pk_fma_f32 v[120:121], v[144:145], s[0:1], v[120:121] op_sel_hi:[1,0,1] neg_lo:[1,0,0] neg_hi:[1,0,0]
	v_sub_f32_e32 v128, v114, v135
	v_pk_fma_f32 v[120:121], v[120:121], v[120:121], v[164:165]
	v_mov_b32_e32 v164, v18
	v_mov_b32_e32 v165, v114
	v_pk_fma_f32 v[164:165], v[144:145], s[0:1], v[164:165] op_sel_hi:[1,0,1] neg_lo:[1,0,0] neg_hi:[1,0,0]
	v_mov_b32_e32 v114, v19
	v_sub_f32_e32 v127, v115, v135
	v_pk_fma_f32 v[120:121], v[164:165], v[164:165], v[120:121]
	v_pk_fma_f32 v[114:115], v[144:145], s[0:1], v[114:115] op_sel_hi:[1,0,1] neg_lo:[1,0,0] neg_hi:[1,0,0]
	v_sub_f32_e32 v126, v116, v135
	v_pk_fma_f32 v[114:115], v[114:115], v[114:115], v[120:121]
	v_mov_b32_e32 v120, v20
	v_mov_b32_e32 v121, v116
	v_pk_fma_f32 v[120:121], v[144:145], s[0:1], v[120:121] op_sel_hi:[1,0,1] neg_lo:[1,0,0] neg_hi:[1,0,0]
	v_mov_b32_e32 v116, v21
	v_sub_f32_e32 v154, v125, v135
	v_sub_f32_e32 v125, v117, v135
	v_pk_fma_f32 v[114:115], v[120:121], v[120:121], v[114:115]
	v_pk_fma_f32 v[116:117], v[144:145], s[0:1], v[116:117] op_sel_hi:[1,0,1] neg_lo:[1,0,0] neg_hi:[1,0,0]
	v_sub_f32_e32 v124, v106, v135
	v_pk_fma_f32 v[114:115], v[116:117], v[116:117], v[114:115]
	v_mov_b32_e32 v116, v14
	v_mov_b32_e32 v117, v106
	v_pk_fma_f32 v[116:117], v[144:145], s[0:1], v[116:117] op_sel_hi:[1,0,1] neg_lo:[1,0,0] neg_hi:[1,0,0]
	v_mov_b32_e32 v106, v15
	v_sub_f32_e32 v123, v107, v135
	v_pk_fma_f32 v[114:115], v[116:117], v[116:117], v[114:115]
	v_pk_fma_f32 v[106:107], v[144:145], s[0:1], v[106:107] op_sel_hi:[1,0,1] neg_lo:[1,0,0] neg_hi:[1,0,0]
	v_sub_f32_e32 v122, v108, v135
	v_pk_fma_f32 v[106:107], v[106:107], v[106:107], v[114:115]
	v_mov_b32_e32 v114, v16
	v_mov_b32_e32 v115, v108
	v_pk_fma_f32 v[114:115], v[144:145], s[0:1], v[114:115] op_sel_hi:[1,0,1] neg_lo:[1,0,0] neg_hi:[1,0,0]
	v_mov_b32_e32 v108, v17
	v_pk_fma_f32 v[106:107], v[114:115], v[114:115], v[106:107]
	v_pk_fma_f32 v[114:115], v[144:145], s[0:1], v[108:109] op_sel_hi:[1,0,1] neg_lo:[1,0,0] neg_hi:[1,0,0]
	v_sub_f32_e32 v119, v110, v135
	v_pk_fma_f32 v[106:107], v[114:115], v[114:115], v[106:107]
	v_mov_b32_e32 v114, v10
	v_mov_b32_e32 v115, v110
	v_pk_fma_f32 v[114:115], v[144:145], s[0:1], v[114:115] op_sel_hi:[1,0,1] neg_lo:[1,0,0] neg_hi:[1,0,0]
	v_mov_b32_e32 v110, v11
	v_pk_fma_f32 v[106:107], v[114:115], v[114:115], v[106:107]
	v_pk_fma_f32 v[114:115], v[144:145], s[0:1], v[110:111] op_sel_hi:[1,0,1] neg_lo:[1,0,0] neg_hi:[1,0,0]
	v_sub_f32_e32 v118, v112, v135
	v_pk_fma_f32 v[106:107], v[114:115], v[114:115], v[106:107]
	v_mov_b32_e32 v114, v12
	v_mov_b32_e32 v115, v112
	v_pk_fma_f32 v[114:115], v[144:145], s[0:1], v[114:115] op_sel_hi:[1,0,1] neg_lo:[1,0,0] neg_hi:[1,0,0]
	v_mov_b32_e32 v112, v13
	v_pk_fma_f32 v[106:107], v[114:115], v[114:115], v[106:107]
	v_pk_fma_f32 v[114:115], v[144:145], s[0:1], v[112:113] op_sel_hi:[1,0,1] neg_lo:[1,0,0] neg_hi:[1,0,0]
	v_pk_add_f32 v[136:137], v[102:103], v[134:135] op_sel:[0,1] neg_lo:[0,1] neg_hi:[0,1]
	v_pk_fma_f32 v[106:107], v[114:115], v[114:115], v[106:107]
	v_pk_add_f32 v[114:115], v[6:7], v[134:135] op_sel_hi:[1,0] neg_lo:[0,1] neg_hi:[0,1]
	v_pk_mul_f32 v[142:143], v[136:137], v[136:137]
	v_pk_mul_f32 v[114:115], v[114:115], v[114:115]
	v_mov_b32_e32 v117, v142
	v_mov_b32_e32 v116, v114
	v_pk_add_f32 v[136:137], v[104:105], v[134:135] op_sel:[0,1] neg_lo:[0,1] neg_hi:[0,1]
	v_pk_add_f32 v[106:107], v[116:117], v[106:107]
	v_pk_add_f32 v[116:117], v[8:9], v[134:135] op_sel_hi:[1,0] neg_lo:[0,1] neg_hi:[0,1]
	v_pk_mul_f32 v[140:141], v[136:137], v[136:137]
	v_pk_mul_f32 v[116:117], v[116:117], v[116:117]
	v_mov_b32_e32 v142, v115
	v_pk_add_f32 v[136:137], v[98:99], v[134:135] op_sel:[0,1] neg_lo:[0,1] neg_hi:[0,1]
	v_pk_add_f32 v[120:121], v[2:3], v[134:135] op_sel_hi:[1,0] neg_lo:[0,1] neg_hi:[0,1]
	v_pk_add_f32 v[106:107], v[142:143], v[106:107]
	v_mov_b32_e32 v114, v116
	v_mov_b32_e32 v115, v140
	v_pk_mul_f32 v[138:139], v[136:137], v[136:137]
	v_pk_mul_f32 v[120:121], v[120:121], v[120:121]
	v_pk_add_f32 v[106:107], v[114:115], v[106:107]
	v_mov_b32_e32 v140, v117
	v_pk_add_f32 v[136:137], v[100:101], v[134:135] op_sel:[0,1] neg_lo:[0,1] neg_hi:[0,1]
	v_pk_add_f32 v[144:145], v[4:5], v[134:135] op_sel_hi:[1,0] neg_lo:[0,1] neg_hi:[0,1]
	v_pk_add_f32 v[106:107], v[140:141], v[106:107]
	v_mov_b32_e32 v114, v120
	v_mov_b32_e32 v115, v138
	v_pk_mul_f32 v[136:137], v[136:137], v[136:137]
	v_pk_mul_f32 v[144:145], v[144:145], v[144:145]
	v_pk_add_f32 v[106:107], v[114:115], v[106:107]
	v_mov_b32_e32 v138, v121
	v_pk_add_f32 v[106:107], v[138:139], v[106:107]
	v_mov_b32_e32 v114, v144
	v_mov_b32_e32 v115, v136
	v_pk_add_f32 v[106:107], v[114:115], v[106:107]
	v_mov_b32_e32 v136, v145
	v_pk_add_f32 v[106:107], v[136:137], v[106:107]
	ds_bpermute_b32 v115, v149, v107
	ds_bpermute_b32 v114, v149, v106
	v_sub_f32_e32 v121, v109, v135
	v_sub_f32_e32 v116, v102, v135
	v_sub_f32_e32 v112, v98, v135
	v_sub_f32_e32 v120, v111, v135
	s_waitcnt lgkmcnt(0)
	v_pk_add_f32 v[106:107], v[106:107], v[114:115]
	ds_bpermute_b32 v109, v148, v107
	ds_bpermute_b32 v108, v148, v106
	v_sub_f32_e32 v115, v103, v135
	v_sub_f32_e32 v111, v99, v135
	v_sub_f32_e32 v114, v104, v135
	v_lshl_add_u32 v152, v82, 3, v85
	s_waitcnt lgkmcnt(0)
	v_pk_add_f32 v[102:103], v[106:107], v[108:109]
	v_mov_b32_e32 v106, 0x3727c5ac
	v_pk_fma_f32 v[108:109], v[102:103], s[0:1], v[106:107] op_sel_hi:[1,0,0]
	s_mov_b32 s1, 0x800000
	v_mul_f32_e32 v98, 0x4b800000, v109
	v_cmp_gt_f32_e32 vcc, s1, v109
	v_sub_f32_e32 v107, v101, v135
	ds_read_b128 v[82:85], v150 offset:17984
	v_cndmask_b32_e32 v98, v109, v98, vcc
	v_rsq_f32_e32 v98, v98
	v_sub_f32_e32 v109, v100, v135
	ds_read_b128 v[86:89], v150 offset:18496
	v_sub_f32_e32 v117, v113, v135
	v_mul_f32_e32 v99, 0x45800000, v98
	v_cndmask_b32_e32 v110, v98, v99, vcc
	v_mul_f32_e32 v112, v110, v112
	v_fma_f32 v34, v34, v112, v38
	v_mul_f32_e32 v38, v110, v111
	v_fma_f32 v35, v35, v38, v39
	v_max_f32_e32 v38, 0, v35
	v_mul_f32_e32 v35, v110, v109
	v_mul_f32_e32 v116, v110, v116
	v_fma_f32 v35, v36, v35, v40
	v_mul_f32_e32 v36, v110, v107
	v_fma_f32 v42, v42, v116, v46
	v_mul_f32_e32 v46, v110, v115
	v_fmac_f32_e32 v41, v37, v36
	v_mul_f32_e32 v37, 0x4b800000, v108
	v_cmp_gt_f32_e32 vcc, s1, v108
	v_sub_f32_e32 v113, v105, v135
	v_fma_f32 v43, v43, v46, v47
	v_mul_f32_e32 v46, v110, v114
	v_cndmask_b32_e32 v37, v108, v37, vcc
	v_mul_f32_e32 v135, v110, v163
	v_fma_f32 v44, v44, v46, v48
	v_mul_f32_e32 v46, v110, v113
	v_rsq_f32_e32 v37, v37
	v_fma_f32 v90, v90, v135, v94
	v_mul_f32_e32 v94, v110, v162
	v_fmac_f32_e32 v49, v45, v46
	ds_read_b128 v[98:101], v150 offset:17920
	ds_read_b128 v[102:105], v150 offset:18432
	v_fma_f32 v91, v91, v94, v95
	v_mul_f32_e32 v94, v110, v161
	v_max_f32_e32 v42, 0, v42
	v_max_f32_e32 v43, 0, v43
	v_max_f32_e32 v44, 0, v44
	v_max_f32_e32 v45, 0, v49
	v_max_f32_e32 v34, 0, v34
	v_max_f32_e32 v35, 0, v35
	v_max_f32_e32 v36, 0, v41
	v_fma_f32 v92, v92, v94, v96
	v_mul_f32_e32 v94, v110, v160
	v_mul_f32_e32 v135, v110, v159
	v_cvt_pk_f16_f32 v115, v44, v45
	v_cvt_pk_f16_f32 v114, v42, v43
	v_cvt_pk_f16_f32 v35, v35, v36
	v_cvt_pk_f16_f32 v34, v34, v38
	v_fmac_f32_e32 v97, v93, v94
	s_waitcnt lgkmcnt(2)
	v_fma_f32 v82, v82, v135, v86
	v_mul_f32_e32 v86, v110, v158
	ds_write2_b64 v152, v[114:115], v[34:35] offset0:24 offset1:28
	v_mul_f32_e32 v34, 0x45800000, v37
	ds_read_b128 v[66:69], v150 offset:18048
	ds_read_b128 v[70:73], v150 offset:18560
	v_max_f32_e32 v90, 0, v90
	v_max_f32_e32 v91, 0, v91
	v_max_f32_e32 v92, 0, v92
	v_max_f32_e32 v93, 0, v97
	v_fma_f32 v83, v83, v86, v87
	v_cndmask_b32_e32 v34, v37, v34, vcc
	v_sub_f32_e32 v31, v31, v134
	v_cvt_pk_f16_f32 v137, v92, v93
	v_cvt_pk_f16_f32 v136, v90, v91
	ds_read_b128 v[90:93], v150 offset:17984
	ds_read_b128 v[94:97], v150 offset:18496
	v_max_f32_e32 v86, 0, v83
	v_mul_f32_e32 v83, v110, v156
	v_mul_f32_e32 v31, v34, v31
	v_fma_f32 v83, v84, v83, v88
	v_mul_f32_e32 v84, v110, v154
	s_waitcnt lgkmcnt(5)
	v_fma_f32 v31, v99, v31, v103
	ds_read_b128 v[50:53], v150 offset:18112
	ds_read_b128 v[54:57], v150 offset:18624
	v_fmac_f32_e32 v89, v85, v84
	v_max_f32_e32 v35, 0, v31
	v_sub_f32_e32 v31, v32, v134
	v_sub_f32_e32 v32, v33, v134
	v_max_f32_e32 v82, 0, v82
	v_max_f32_e32 v83, 0, v83
	v_max_f32_e32 v84, 0, v89
	v_mul_f32_e32 v135, v110, v153
	v_mul_f32_e32 v31, v34, v31
	v_mul_f32_e32 v32, v34, v32
	v_sub_f32_e32 v27, v27, v134
	v_cvt_pk_f16_f32 v83, v83, v84
	v_cvt_pk_f16_f32 v82, v82, v86
	s_waitcnt lgkmcnt(4)
	v_fma_f32 v66, v66, v135, v70
	v_mul_f32_e32 v70, v110, v157
	v_fma_f32 v31, v100, v31, v104
	v_fmac_f32_e32 v105, v101, v32
	v_mul_f32_e32 v27, v34, v27
	ds_write2_b64 v152, v[136:137], v[82:83] offset1:4
	ds_read_b128 v[82:85], v150 offset:18048
	ds_read_b128 v[86:89], v150 offset:18560
	v_fma_f32 v67, v67, v70, v71
	v_mul_f32_e32 v70, v110, v155
	v_max_f32_e32 v31, 0, v31
	v_max_f32_e32 v32, 0, v105
	s_waitcnt lgkmcnt(5)
	v_fma_f32 v27, v91, v27, v95
	v_fma_f32 v68, v68, v70, v72
	v_mul_f32_e32 v70, v110, v129
	v_mul_f32_e32 v128, v110, v128
	v_sub_f32_e32 v30, v30, v134
	v_cvt_pk_f16_f32 v31, v31, v32
	v_sub_f32_e32 v26, v26, v134
	v_max_f32_e32 v32, 0, v27
	v_sub_f32_e32 v27, v28, v134
	v_sub_f32_e32 v28, v29, v134
	v_fmac_f32_e32 v73, v69, v70
	s_waitcnt lgkmcnt(3)
	v_fma_f32 v50, v50, v128, v54
	v_mul_f32_e32 v54, v110, v127
	v_mul_f32_e32 v30, v34, v30
	v_mul_f32_e32 v26, v34, v26
	v_mul_f32_e32 v27, v34, v27
	v_mul_f32_e32 v28, v34, v28
	ds_read_b128 v[74:77], v150 offset:18176
	ds_read_b128 v[78:81], v150 offset:18688
	v_max_f32_e32 v66, 0, v66
	v_max_f32_e32 v67, 0, v67
	v_max_f32_e32 v68, 0, v68
	v_max_f32_e32 v69, 0, v73
	v_fma_f32 v51, v51, v54, v55
	v_fma_f32 v30, v98, v30, v102
	v_fma_f32 v26, v90, v26, v94
	v_fma_f32 v27, v92, v27, v96
	v_fmac_f32_e32 v97, v93, v28
	v_sub_f32_e32 v23, v23, v134
	v_cvt_pk_f16_f32 v137, v68, v69
	v_cvt_pk_f16_f32 v136, v66, v67
	ds_read_b128 v[66:69], v150 offset:18112
	ds_read_b128 v[70:73], v150 offset:18624
	v_max_f32_e32 v54, 0, v51
	v_mul_f32_e32 v51, v110, v126
	v_max_f32_e32 v30, 0, v30
	v_max_f32_e32 v26, 0, v26
	v_max_f32_e32 v27, 0, v27
	v_max_f32_e32 v28, 0, v97
	v_mul_f32_e32 v23, v34, v23
	v_fma_f32 v51, v52, v51, v56
	v_mul_f32_e32 v52, v110, v125
	v_cvt_pk_f16_f32 v30, v30, v35
	v_cvt_pk_f16_f32 v27, v27, v28
	v_cvt_pk_f16_f32 v26, v26, v32
	v_add_u32_e32 v28, 0x1000, v152
	s_waitcnt lgkmcnt(4)
	v_fma_f32 v23, v83, v23, v87
	ds_read_b128 v[58:61], v150 offset:18240
	ds_read_b128 v[62:65], v150 offset:18752
	v_fmac_f32_e32 v57, v53, v52
	ds_write2_b64 v28, v[30:31], v[26:27] offset0:32 offset1:36
	v_max_f32_e32 v26, 0, v23
	v_sub_f32_e32 v23, v24, v134
	v_sub_f32_e32 v24, v25, v134
	v_max_f32_e32 v50, 0, v50
	v_max_f32_e32 v51, 0, v51
	v_max_f32_e32 v52, 0, v57
	v_mul_f32_e32 v124, v110, v124
	v_mul_f32_e32 v23, v34, v23
	v_mul_f32_e32 v24, v34, v24
	v_sub_f32_e32 v19, v19, v134
	v_cvt_pk_f16_f32 v51, v51, v52
	v_cvt_pk_f16_f32 v50, v50, v54
	s_waitcnt lgkmcnt(5)
	v_fma_f32 v74, v74, v124, v78
	v_mul_f32_e32 v78, v110, v123
	v_fma_f32 v23, v84, v23, v88
	v_fmac_f32_e32 v89, v85, v24
	v_mul_f32_e32 v19, v34, v19
	ds_write2_b64 v152, v[136:137], v[50:51] offset0:8 offset1:12
	ds_read_b128 v[50:53], v150 offset:18176
	ds_read_b128 v[54:57], v150 offset:18688
	v_fma_f32 v75, v75, v78, v79
	v_mul_f32_e32 v78, v110, v122
	v_max_f32_e32 v23, 0, v23
	v_max_f32_e32 v24, 0, v89
	s_waitcnt lgkmcnt(6)
	v_fma_f32 v19, v67, v19, v71
	v_fma_f32 v76, v76, v78, v80
	v_mul_f32_e32 v78, v110, v121
	v_mul_f32_e32 v119, v110, v119
	v_sub_f32_e32 v22, v22, v134
	v_cvt_pk_f16_f32 v23, v23, v24
	v_sub_f32_e32 v18, v18, v134
	v_max_f32_e32 v24, 0, v19
	v_sub_f32_e32 v19, v20, v134
	v_sub_f32_e32 v20, v21, v134
	v_fmac_f32_e32 v81, v77, v78
	s_waitcnt lgkmcnt(4)
	v_fma_f32 v58, v58, v119, v62
	v_mul_f32_e32 v62, v110, v120
	v_mul_f32_e32 v22, v34, v22
	v_mul_f32_e32 v18, v34, v18
	v_mul_f32_e32 v19, v34, v19
	v_mul_f32_e32 v20, v34, v20
	v_max_f32_e32 v74, 0, v74
	v_max_f32_e32 v75, 0, v75
	v_max_f32_e32 v76, 0, v76
	v_max_f32_e32 v77, 0, v81
	v_fma_f32 v59, v59, v62, v63
	v_fma_f32 v22, v82, v22, v86
	v_fma_f32 v18, v66, v18, v70
	v_fma_f32 v19, v68, v19, v72
	v_fmac_f32_e32 v73, v69, v20
	v_sub_f32_e32 v15, v15, v134
	v_cvt_pk_f16_f32 v123, v76, v77
	v_cvt_pk_f16_f32 v122, v74, v75
	ds_read_b128 v[74:77], v150 offset:18240
	ds_read_b128 v[78:81], v150 offset:18752
	v_max_f32_e32 v62, 0, v59
	v_mul_f32_e32 v59, v110, v118
	v_max_f32_e32 v22, 0, v22
	v_max_f32_e32 v18, 0, v18
	v_max_f32_e32 v19, 0, v19
	v_max_f32_e32 v20, 0, v73
	v_mul_f32_e32 v15, v34, v15
	v_fma_f32 v59, v60, v59, v64
	v_mul_f32_e32 v60, v110, v117
	v_cvt_pk_f16_f32 v22, v22, v26
	v_cvt_pk_f16_f32 v19, v19, v20
	v_cvt_pk_f16_f32 v18, v18, v24
	s_waitcnt lgkmcnt(2)
	v_fma_f32 v15, v51, v15, v55
	v_fmac_f32_e32 v65, v61, v60
	ds_write2_b64 v28, v[22:23], v[18:19] offset0:40 offset1:44
	v_max_f32_e32 v18, 0, v15
	v_sub_f32_e32 v15, v16, v134
	v_sub_f32_e32 v16, v17, v134
	v_max_f32_e32 v58, 0, v58
	v_max_f32_e32 v59, 0, v59
	v_max_f32_e32 v60, 0, v65
	v_mul_f32_e32 v15, v34, v15
	v_mul_f32_e32 v16, v34, v16
	v_sub_f32_e32 v11, v11, v134
	v_cvt_pk_f16_f32 v59, v59, v60
	v_cvt_pk_f16_f32 v58, v58, v62
	v_fma_f32 v15, v52, v15, v56
	v_fmac_f32_e32 v57, v53, v16
	v_mul_f32_e32 v11, v34, v11
	ds_write2_b64 v152, v[122:123], v[58:59] offset0:16 offset1:20
	ds_read_b128 v[58:61], v150 offset:18304
	ds_read_b128 v[62:65], v150 offset:18816
	v_max_f32_e32 v15, 0, v15
	v_max_f32_e32 v16, 0, v57
	s_waitcnt lgkmcnt(4)
	v_fma_f32 v11, v75, v11, v79
	v_sub_f32_e32 v14, v14, v134
	v_cvt_pk_f16_f32 v15, v15, v16
	v_sub_f32_e32 v10, v10, v134
	v_max_f32_e32 v16, 0, v11
	v_sub_f32_e32 v11, v12, v134
	v_sub_f32_e32 v12, v13, v134
	v_mul_f32_e32 v14, v34, v14
	v_mul_f32_e32 v10, v34, v10
	v_mul_f32_e32 v11, v34, v11
	v_mul_f32_e32 v12, v34, v12
	v_fma_f32 v14, v50, v14, v54
	v_fma_f32 v10, v74, v10, v78
	v_fma_f32 v11, v76, v11, v80
	v_fmac_f32_e32 v81, v77, v12
	v_sub_f32_e32 v7, v7, v134
	ds_read_b128 v[42:45], v150 offset:18368
	ds_read_b128 v[46:49], v150 offset:18880
	v_max_f32_e32 v14, 0, v14
	v_max_f32_e32 v10, 0, v10
	v_max_f32_e32 v11, 0, v11
	v_max_f32_e32 v12, 0, v81
	v_mul_f32_e32 v7, v34, v7
	v_cvt_pk_f16_f32 v14, v14, v18
	v_cvt_pk_f16_f32 v11, v11, v12
	v_cvt_pk_f16_f32 v10, v10, v16
	s_waitcnt lgkmcnt(2)
	v_fma_f32 v7, v59, v7, v63
	ds_write2_b64 v28, v[14:15], v[10:11] offset0:48 offset1:52
	v_max_f32_e32 v10, 0, v7
	v_sub_f32_e32 v7, v8, v134
	v_sub_f32_e32 v8, v9, v134
	v_mul_f32_e32 v7, v34, v7
	v_mul_f32_e32 v8, v34, v8
	v_sub_f32_e32 v3, v3, v134
	v_fma_f32 v7, v60, v7, v64
	v_fmac_f32_e32 v65, v61, v8
	v_mul_f32_e32 v3, v34, v3
	v_max_f32_e32 v7, 0, v7
	v_max_f32_e32 v8, 0, v65
	s_waitcnt lgkmcnt(1)
	v_fma_f32 v3, v43, v3, v47
	v_sub_f32_e32 v6, v6, v134
	v_cvt_pk_f16_f32 v7, v7, v8
	v_sub_f32_e32 v2, v2, v134
	v_max_f32_e32 v8, 0, v3
	v_sub_f32_e32 v3, v4, v134
	v_sub_f32_e32 v4, v5, v134
	v_mul_f32_e32 v6, v34, v6
	v_mul_f32_e32 v2, v34, v2
	v_mul_f32_e32 v3, v34, v3
	v_mul_f32_e32 v4, v34, v4
	v_fma_f32 v6, v58, v6, v62
	v_fma_f32 v2, v42, v2, v46
	v_fma_f32 v3, v44, v3, v48
	v_fmac_f32_e32 v49, v45, v4
	v_max_f32_e32 v6, 0, v6
	v_max_f32_e32 v2, 0, v2
	v_max_f32_e32 v3, 0, v3
	v_max_f32_e32 v4, 0, v49
	v_cvt_pk_f16_f32 v6, v6, v10
	v_cvt_pk_f16_f32 v3, v3, v4
	v_cvt_pk_f16_f32 v2, v2, v8
	ds_write2_b64 v28, v[6:7], v[2:3] offset0:56 offset1:60
	v_lshl_add_u64 v[34:35], s[36:37], 0, v[132:133]
	v_add_co_u32_e32 v74, vcc, s9, v34
	global_load_dwordx4 v[66:69], v132, s[36:37]
	s_nop 0
	v_addc_co_u32_e32 v75, vcc, 0, v35, vcc
	v_add_co_u32_e32 v76, vcc, s11, v34
	ds_read_b128 v[116:119], v151
	s_nop 0
	v_addc_co_u32_e32 v77, vcc, 0, v35, vcc
	global_load_dwordx4 v[88:91], v[76:77], off offset:-4096
	v_add_co_u32_e32 v78, vcc, s12, v34
	global_load_dwordx4 v[70:73], v[76:77], off
	s_nop 0
	v_addc_co_u32_e32 v79, vcc, 0, v35, vcc
	v_add_co_u32_e32 v80, vcc, s8, v34
	ds_read_b128 v[120:123], v151 offset:4352
	s_nop 0
	v_addc_co_u32_e32 v81, vcc, 0, v35, vcc
	global_load_dwordx4 v[92:95], v[80:81], off offset:-4096
	v_add_co_u32_e32 v82, vcc, s10, v34
	global_load_dwordx4 v[96:99], v[80:81], off
	s_nop 0
	v_addc_co_u32_e32 v83, vcc, 0, v35, vcc
	v_add_co_u32_e32 v84, vcc, s7, v34
	ds_read_b128 v[164:167], v151 offset:4416
	s_nop 0
	v_addc_co_u32_e32 v85, vcc, 0, v35, vcc
	global_load_dwordx4 v[108:111], v[84:85], off
	global_load_dwordx4 v[100:103], v[84:85], off offset:-4096
	v_add_co_u32_e32 v86, vcc, s6, v34
	s_nop 1
	v_addc_co_u32_e32 v87, vcc, 0, v35, vcc
	global_load_dwordx4 v[112:115], v[86:87], off
	global_load_dwordx4 v[58:61], v132, s[36:37] offset:1024
	global_load_dwordx4 v[62:65], v[74:75], off offset:1024
	global_load_dwordx4 v[34:37], v[76:77], off offset:1024
	global_load_dwordx4 v[54:57], v[78:79], off offset:1024
	global_load_dwordx4 v[50:53], v[80:81], off offset:1024
	global_load_dwordx4 v[46:49], v[82:83], off offset:1024
	global_load_dwordx4 v[42:45], v[84:85], off offset:1024
	global_load_dwordx4 v[38:41], v[86:87], off offset:1024
	ds_read_b128 v[30:33], v147 offset:18944
	ds_read_b128 v[26:29], v147 offset:19008
	s_waitcnt vmcnt(15) lgkmcnt(1)
	v_mfma_f32_16x16x32_f16 v[124:127], v[66:69], v[116:119], v[30:33]
	v_mfma_f32_16x16x32_f16 v[66:69], v[66:69], v[120:123], v[30:33]
	s_waitcnt vmcnt(14) lgkmcnt(0)
	v_mfma_f32_16x16x32_f16 v[134:137], v[88:91], v[116:119], v[26:29]
	v_mfma_f32_16x16x32_f16 v[88:91], v[88:91], v[120:123], v[26:29]
	global_load_dwordx4 v[30:33], v132, s[36:37] offset:2048
	s_nop 1
	global_load_dwordx4 v[26:29], v[74:75], off offset:2048
	ds_read_b128 v[22:25], v147 offset:19072
	ds_read_b128 v[18:21], v147 offset:19136
	s_waitcnt vmcnt(15) lgkmcnt(1)
	v_mfma_f32_16x16x32_f16 v[138:141], v[70:73], v[116:119], v[22:25]
	v_mfma_f32_16x16x32_f16 v[70:73], v[70:73], v[120:123], v[22:25]
	s_waitcnt vmcnt(14) lgkmcnt(0)
	v_mfma_f32_16x16x32_f16 v[142:145], v[92:95], v[116:119], v[18:21]
	v_mfma_f32_16x16x32_f16 v[92:95], v[92:95], v[120:123], v[18:21]
	global_load_dwordx4 v[22:25], v[76:77], off offset:2048
	s_nop 1
	global_load_dwordx4 v[18:21], v[78:79], off offset:2048
	ds_read_b128 v[6:9], v147 offset:19328
	s_waitcnt vmcnt(14) lgkmcnt(0)
	v_mfma_f32_16x16x32_f16 v[160:163], v[108:111], v[116:119], v[6:9]
	v_mfma_f32_16x16x32_f16 v[108:111], v[108:111], v[120:123], v[6:9]
	s_nop 2
	global_load_dwordx4 v[6:9], v[84:85], off offset:2048
	ds_read_b128 v[10:13], v147 offset:19264
	s_waitcnt vmcnt(14) lgkmcnt(0)
	v_mfma_f32_16x16x32_f16 v[156:159], v[100:103], v[116:119], v[10:13]
	v_mfma_f32_16x16x32_f16 v[100:103], v[100:103], v[120:123], v[10:13]
	s_nop 2
	global_load_dwordx4 v[10:13], v[82:83], off offset:2048
	ds_read_b128 v[14:17], v147 offset:19200
	s_waitcnt lgkmcnt(0)
	v_mfma_f32_16x16x32_f16 v[152:155], v[96:99], v[116:119], v[14:17]
	ds_read_b128 v[2:5], v147 offset:19392
	s_waitcnt vmcnt(14) lgkmcnt(0)
	v_mfma_f32_16x16x32_f16 v[116:119], v[112:115], v[116:119], v[2:5]
	v_mfma_f32_16x16x32_f16 v[112:115], v[112:115], v[120:123], v[2:5]
	s_nop 2
	global_load_dwordx4 v[2:5], v[86:87], off offset:2048
	v_mfma_f32_16x16x32_f16 v[96:99], v[96:99], v[120:123], v[14:17]
	ds_read_b128 v[120:123], v151 offset:64
	s_nop 1
	global_load_dwordx4 v[14:17], v[80:81], off offset:2048
	s_waitcnt vmcnt(15) lgkmcnt(0)
	v_mfma_f32_16x16x32_f16 v[124:127], v[58:61], v[120:123], v[124:127]
	v_mfma_f32_16x16x32_f16 v[58:61], v[58:61], v[164:167], v[66:69]
	s_waitcnt vmcnt(14)
	v_mfma_f32_16x16x32_f16 v[66:69], v[62:65], v[120:123], v[134:137]
	v_mfma_f32_16x16x32_f16 v[62:65], v[62:65], v[164:167], v[88:91]
	s_nop 1
	global_load_dwordx4 v[134:137], v[82:83], off offset:3072
	s_nop 0
	global_load_dwordx4 v[82:85], v[84:85], off offset:3072
	s_waitcnt vmcnt(15)
	v_mfma_f32_16x16x32_f16 v[88:91], v[34:37], v[120:123], v[138:141]
	v_mfma_f32_16x16x32_f16 v[34:37], v[34:37], v[164:167], v[70:73]
	s_nop 1
	global_load_dwordx4 v[138:141], v[86:87], off offset:3072
	s_waitcnt vmcnt(15)
	v_mfma_f32_16x16x32_f16 v[70:73], v[54:57], v[120:123], v[142:145]
	v_mfma_f32_16x16x32_f16 v[54:57], v[54:57], v[164:167], v[92:95]
	s_nop 1
	ds_read_b128 v[142:145], v151 offset:128
	s_waitcnt vmcnt(14)
	v_mfma_f32_16x16x32_f16 v[92:95], v[50:53], v[120:123], v[152:155]
	v_mfma_f32_16x16x32_f16 v[50:53], v[50:53], v[164:167], v[96:99]
	s_nop 1
	ds_read_b128 v[152:155], v151 offset:4480
	s_waitcnt vmcnt(13)
	v_mfma_f32_16x16x32_f16 v[96:99], v[46:49], v[120:123], v[156:159]
	v_mfma_f32_16x16x32_f16 v[46:49], v[46:49], v[164:167], v[100:103]
	s_waitcnt vmcnt(12)
	v_mfma_f32_16x16x32_f16 v[100:103], v[42:45], v[120:123], v[160:163]
	v_mfma_f32_16x16x32_f16 v[42:45], v[42:45], v[164:167], v[108:111]
	s_waitcnt vmcnt(11)
	v_mfma_f32_16x16x32_f16 v[108:111], v[38:41], v[120:123], v[116:119]
	global_load_dwordx4 v[120:123], v[78:79], off offset:3072
	s_nop 0
	global_load_dwordx4 v[78:81], v[80:81], off offset:3072
	s_nop 0
	global_load_dwordx4 v[116:119], v[74:75], off offset:3072
	v_mfma_f32_16x16x32_f16 v[38:41], v[38:41], v[164:167], v[112:115]
	global_load_dwordx4 v[74:77], v[76:77], off offset:3072
	s_nop 1
	global_load_dwordx4 v[112:115], v132, s[36:37] offset:3072
	s_waitcnt vmcnt(15) lgkmcnt(1)
	v_mfma_f32_16x16x32_f16 v[124:127], v[30:33], v[142:145], v[124:127]
	s_waitcnt lgkmcnt(0)
	v_mfma_f32_16x16x32_f16 v[30:33], v[30:33], v[152:155], v[58:61]
	s_waitcnt vmcnt(14)
	v_mfma_f32_16x16x32_f16 v[58:61], v[26:29], v[142:145], v[66:69]
	v_mfma_f32_16x16x32_f16 v[26:29], v[26:29], v[152:155], v[62:65]
	s_waitcnt vmcnt(13)
	v_mfma_f32_16x16x32_f16 v[62:65], v[22:25], v[142:145], v[88:91]
	v_mfma_f32_16x16x32_f16 v[22:25], v[22:25], v[152:155], v[34:37]
	s_waitcnt vmcnt(12)
	v_mfma_f32_16x16x32_f16 v[34:37], v[18:21], v[142:145], v[70:73]
	s_waitcnt vmcnt(8)
	v_mfma_f32_16x16x32_f16 v[66:69], v[14:17], v[142:145], v[92:95]
	v_mfma_f32_16x16x32_f16 v[86:89], v[10:13], v[142:145], v[96:99]
	v_mfma_f32_16x16x32_f16 v[94:97], v[6:9], v[142:145], v[100:103]
	v_mfma_f32_16x16x32_f16 v[102:105], v[2:5], v[142:145], v[108:111]
	ds_read_b128 v[142:145], v151 offset:4544
	s_nop 1
	ds_read_b128 v[108:111], v151 offset:192
	v_mfma_f32_16x16x32_f16 v[18:21], v[18:21], v[152:155], v[54:57]
	v_mfma_f32_16x16x32_f16 v[70:73], v[14:17], v[152:155], v[50:53]
	v_mfma_f32_16x16x32_f16 v[90:93], v[10:13], v[152:155], v[46:49]
	v_mfma_f32_16x16x32_f16 v[98:101], v[6:9], v[152:155], v[42:45]
	v_mfma_f32_16x16x32_f16 v[2:5], v[2:5], v[152:155], v[38:41]
	s_waitcnt vmcnt(0) lgkmcnt(1)
	v_mfma_f32_16x16x32_f16 v[6:9], v[112:115], v[142:145], v[30:33]
	s_waitcnt lgkmcnt(0)
	v_mfma_f32_16x16x32_f16 v[50:53], v[116:119], v[108:111], v[58:61]
	v_mfma_f32_16x16x32_f16 v[10:13], v[116:119], v[142:145], v[26:29]
	v_mfma_f32_16x16x32_f16 v[54:57], v[74:77], v[108:111], v[62:65]
	v_mfma_f32_16x16x32_f16 v[14:17], v[74:77], v[142:145], v[22:25]
	v_mfma_f32_16x16x32_f16 v[18:21], v[120:123], v[142:145], v[18:21]
	v_mfma_f32_16x16x32_f16 v[22:25], v[78:81], v[142:145], v[70:73]
	v_mfma_f32_16x16x32_f16 v[26:29], v[134:137], v[142:145], v[90:93]
	v_mfma_f32_16x16x32_f16 v[30:33], v[82:85], v[142:145], v[98:101]
	v_mfma_f32_16x16x32_f16 v[2:5], v[138:141], v[142:145], v[2:5]
	v_mfma_f32_16x16x32_f16 v[46:49], v[112:115], v[108:111], v[124:127]
	v_mfma_f32_16x16x32_f16 v[58:61], v[120:123], v[108:111], v[34:37]
	v_mfma_f32_16x16x32_f16 v[62:65], v[78:81], v[108:111], v[66:69]
	v_mfma_f32_16x16x32_f16 v[42:45], v[134:137], v[108:111], v[86:89]
	v_mfma_f32_16x16x32_f16 v[38:41], v[82:85], v[108:111], v[94:97]
	v_mfma_f32_16x16x32_f16 v[34:37], v[138:141], v[108:111], v[102:105]
	s_nop 2
	v_lshrrev_b32_e32 v104, 5, v146
	v_lshlrev_b32_e32 v66, 2, v104
	v_lshl_or_b32 v105, v1, 7, v66
	ds_read_b32 v70, v105 offset:20480
	ds_read_b128 v[112:115], v150 offset:19776
	v_add_u32_e32 v82, 0x5000, v105
	ds_read2_b32 v[68:69], v82 offset1:2
	ds_read2_b32 v[78:79], v82 offset0:4 offset1:6
	v_lshlrev_b32_e32 v0, 4, v0
	v_and_b32_e32 v132, 0x1f0, v0
	v_lshl_add_u64 v[66:67], s[4:5], 0, v[132:133]
	v_add_u32_e32 v83, v130, v132
	v_lshl_add_u64 v[0:1], s[2:3], 0, v[132:133]
	ds_read2_b32 v[80:81], v82 offset0:8 offset1:10
	s_waitcnt lgkmcnt(4)
	v_max_i32_e32 v132, 0, v70
	v_lshlrev_b64 v[70:71], 9, v[132:133]
	s_waitcnt lgkmcnt(2)
	v_max_i32_e32 v132, 0, v69
	v_lshlrev_b64 v[72:73], 9, v[132:133]
	s_waitcnt lgkmcnt(1)
	v_max_i32_e32 v132, 0, v78
	v_lshlrev_b64 v[84:85], 9, v[132:133]
	v_max_i32_e32 v132, 0, v79
	v_lshlrev_b64 v[78:79], 9, v[132:133]
	v_lshl_add_u64 v[84:85], v[66:67], 0, v[84:85]
	v_lshl_add_u64 v[78:79], v[66:67], 0, v[78:79]
	s_waitcnt lgkmcnt(0)
	v_max_i32_e32 v132, 0, v80
	global_load_dwordx4 v[84:87], v[84:85], off nt
	v_lshl_add_u64 v[70:71], v[66:67], 0, v[70:71]
	global_load_dwordx4 v[88:91], v[78:79], off nt
	v_lshlrev_b64 v[78:79], 9, v[132:133]
	v_max_i32_e32 v132, 0, v81
	ds_read2_b32 v[80:81], v82 offset0:12 offset1:14
	v_lshlrev_b64 v[92:93], 9, v[132:133]
	v_lshl_add_u64 v[78:79], v[66:67], 0, v[78:79]
	v_lshl_add_u64 v[96:97], v[66:67], 0, v[92:93]
	global_load_dwordx4 v[92:95], v[78:79], off nt
	s_waitcnt lgkmcnt(0)
	v_max_i32_e32 v132, 0, v80
	global_load_dwordx4 v[96:99], v[96:97], off nt
	v_lshlrev_b64 v[78:79], 9, v[132:133]
	v_max_i32_e32 v132, 0, v81
	v_lshlrev_b64 v[80:81], 9, v[132:133]
	v_lshl_add_u64 v[74:75], v[66:67], 0, v[72:73]
	v_lshl_add_u64 v[78:79], v[66:67], 0, v[78:79]
	v_lshl_add_u64 v[80:81], v[66:67], 0, v[80:81]
	global_load_dwordx4 v[70:73], v[70:71], off nt
	s_movk_i32 s2, 0x220
	global_load_dwordx4 v[74:77], v[74:75], off nt
	v_mov_b32_e32 v69, 0x440
	global_load_dwordx4 v[100:103], v[78:79], off nt
	global_load_dwordx4 v[108:111], v[80:81], off nt
	v_mov_b32_e32 v78, 0x880
	v_mad_u32_u24 v69, v104, s2, v69
	v_mad_u32_u24 v78, v104, s2, v78
	v_mad_u32_u24 v107, v131, s2, v130
	v_mad_u32_u24 v79, v104, s2, v83
	v_add_u32_e32 v81, v83, v69
	v_add_u32_e32 v80, v83, v78
	v_add_u32_e32 v82, v107, v147
	s_load_dword s0, s[34:35], 0x0
	v_mul_u32_u24_e32 v69, 0x220, v104
	ds_read_b128 v[120:123], v150 offset:20288
	ds_read_b128 v[128:131], v150 offset:20352
	ds_read_b128 v[134:137], v150 offset:20416
	ds_read_b128 v[116:119], v150 offset:20224
	ds_read_b128 v[124:127], v150 offset:19904
	s_waitcnt vmcnt(7)
	ds_write_b128 v80, v[84:87]
	s_waitcnt vmcnt(6)
	ds_write_b128 v80, v[88:91] offset:1088
	s_waitcnt vmcnt(5)
	ds_write_b128 v80, v[92:95] offset:2176
	s_waitcnt vmcnt(4)
	ds_write_b128 v80, v[96:99] offset:3264
	s_waitcnt vmcnt(3)
	ds_write_b128 v79, v[70:73]
	s_waitcnt vmcnt(2)
	ds_write_b128 v81, v[74:77]
	s_waitcnt vmcnt(1)
	ds_write_b128 v80, v[100:103] offset:4352
	s_waitcnt vmcnt(0)
	ds_write_b128 v80, v[108:111] offset:5440
	ds_read_b128 v[70:73], v82
	ds_read_b128 v[84:87], v82 offset:64
	ds_read_b128 v[88:91], v82 offset:128
	ds_read_b128 v[92:95], v82 offset:192
	ds_read_b128 v[96:99], v82 offset:256
	ds_read_b128 v[100:103], v82 offset:320
	s_waitcnt lgkmcnt(0)
	v_pk_fma_f32 v[78:79], s[0:1], v[46:47], v[70:71] op_sel_hi:[0,1,1]
	v_pk_fma_f32 v[76:77], s[0:1], v[48:49], v[72:73] op_sel_hi:[0,1,1]
	v_pk_fma_f32 v[74:75], s[0:1], v[50:51], v[84:85] op_sel_hi:[0,1,1]
	v_pk_fma_f32 v[72:73], s[0:1], v[52:53], v[86:87] op_sel_hi:[0,1,1]
	v_pk_fma_f32 v[70:71], s[0:1], v[54:55], v[88:89] op_sel_hi:[0,1,1]
	v_pk_fma_f32 v[54:55], s[0:1], v[56:57], v[90:91] op_sel_hi:[0,1,1]
	v_pk_fma_f32 v[52:53], s[0:1], v[58:59], v[92:93] op_sel_hi:[0,1,1]
	v_pk_fma_f32 v[50:51], s[0:1], v[60:61], v[94:95] op_sel_hi:[0,1,1]
	v_pk_fma_f32 v[48:49], s[0:1], v[62:63], v[96:97] op_sel_hi:[0,1,1]
	v_mov_b32_e32 v56, v78
	v_mov_b32_e32 v57, v74
	v_mov_b32_e32 v58, v79
	v_mov_b32_e32 v59, v75
	v_mov_b32_e32 v60, v76
	v_mov_b32_e32 v61, v72
	v_mov_b32_e32 v62, v77
	v_mov_b32_e32 v63, v73
	v_pk_fma_f32 v[46:47], s[0:1], v[64:65], v[98:99] op_sel_hi:[0,1,1]
	v_mov_b32_e32 v64, v70
	v_mov_b32_e32 v65, v54
	v_mov_b32_e32 v84, v71
	v_mov_b32_e32 v85, v55
	v_pk_add_f32 v[56:57], v[56:57], v[58:59]
	v_pk_add_f32 v[58:59], v[60:61], v[62:63]
	v_pk_add_f32 v[60:61], v[64:65], v[84:85]
	v_pk_add_f32 v[56:57], v[56:57], v[58:59]
	v_pk_add_f32 v[86:87], v[52:53], v[52:53] op_sel:[0,1] op_sel_hi:[1,0]
	v_pk_add_f32 v[88:89], v[50:51], v[50:51] op_sel:[0,1] op_sel_hi:[1,0]
	v_pk_add_f32 v[58:59], v[60:61], v[60:61] op_sel:[0,1] op_sel_hi:[1,0]
	v_add_f32_e32 v56, 0, v56
	v_mov_b32_e32 v91, v48
	v_mov_b32_e32 v87, v46
	v_mov_b32_e32 v89, v47
	v_mov_b32_e32 v59, v49
	v_add_f32_e32 v90, v56, v57
	v_pk_fma_f32 v[42:43], s[0:1], v[42:43], v[100:101] op_sel_hi:[0,1,1]
	v_pk_fma_f32 v[44:45], s[0:1], v[44:45], v[102:103] op_sel_hi:[0,1,1]
	v_pk_add_f32 v[60:61], v[86:87], v[88:89]
	v_pk_add_f32 v[56:57], v[90:91], v[58:59]
	v_mov_b32_e32 v92, v42
	v_pk_add_f32 v[56:57], v[56:57], v[60:61]
	v_mov_b32_e32 v93, v44
	v_mov_b32_e32 v60, v43
	v_mov_b32_e32 v61, v45
	v_pk_add_f32 v[64:65], v[56:57], v[56:57] op_sel:[0,1] op_sel_hi:[1,0]
	ds_read_b128 v[56:59], v82 offset:384
	v_pk_add_f32 v[60:61], v[92:93], v[60:61]
	ds_read_b128 v[96:99], v150 offset:20096
	v_pk_add_f32 v[84:85], v[60:61], v[60:61] op_sel:[0,1] op_sel_hi:[1,0]
	ds_read_b128 v[60:63], v82 offset:448
	s_waitcnt lgkmcnt(2)
	v_pk_fma_f32 v[88:89], s[0:1], v[38:39], v[56:57] op_sel_hi:[0,1,1]
	v_pk_fma_f32 v[40:41], s[0:1], v[40:41], v[58:59] op_sel_hi:[0,1,1]
	v_pk_add_f32 v[38:39], v[88:89], v[88:89] op_sel:[0,1] op_sel_hi:[1,0]
	v_pk_add_f32 v[56:57], v[40:41], v[40:41] op_sel:[0,1] op_sel_hi:[1,0]
	s_waitcnt lgkmcnt(0)
	v_pk_fma_f32 v[90:91], s[0:1], v[34:35], v[60:61] op_sel_hi:[0,1,1]
	v_pk_fma_f32 v[92:93], s[0:1], v[36:37], v[62:63] op_sel_hi:[0,1,1]
	v_mov_b32_e32 v65, v90
	v_mov_b32_e32 v85, v91
	v_mov_b32_e32 v39, v92
	v_mov_b32_e32 v57, v93
	v_pk_add_f32 v[34:35], v[64:65], v[84:85]
	v_pk_add_f32 v[36:37], v[38:39], v[56:57]
	ds_read_b128 v[62:65], v150 offset:19968
	v_pk_add_f32 v[34:35], v[34:35], v[36:37]
	ds_read_b128 v[36:39], v150 offset:19456
	ds_read_b128 v[58:61], v150 offset:19520
	v_add_f32_e32 v34, v34, v35
	ds_bpermute_b32 v35, v149, v34
	ds_read_b128 v[84:87], v150 offset:20032
	v_add_u32_e32 v57, v107, v150
	ds_read_b128 v[100:103], v150 offset:20160
	ds_read_b128 v[108:111], v150 offset:19712
	s_waitcnt lgkmcnt(3)
	v_add_f32_e32 v34, v34, v35
	ds_bpermute_b32 v35, v148, v34
	v_or_b32_e32 v56, 0x5000, v105
	s_waitcnt lgkmcnt(0)
	v_add_f32_e32 v35, v34, v35
	v_fmamk_f32 v95, v35, 0xbc000000, v79
	v_fmamk_f32 v94, v35, 0xbc000000, v78
	v_mul_f32_e32 v95, v95, v95
	v_fmac_f32_e32 v95, v94, v94
	v_fmamk_f32 v94, v35, 0xbc000000, v76
	v_fmac_f32_e32 v95, v94, v94
	v_fmamk_f32 v94, v35, 0xbc000000, v77
	v_fmac_f32_e32 v95, v94, v94
	v_fmamk_f32 v94, v35, 0xbc000000, v74
	v_fmac_f32_e32 v95, v94, v94
	v_fmamk_f32 v94, v35, 0xbc000000, v75
	v_fmac_f32_e32 v95, v94, v94
	v_fmamk_f32 v94, v35, 0xbc000000, v72
	v_fmac_f32_e32 v95, v94, v94
	v_fmamk_f32 v94, v35, 0xbc000000, v73
	v_fmac_f32_e32 v95, v94, v94
	v_fmamk_f32 v94, v35, 0xbc000000, v70
	v_fmac_f32_e32 v95, v94, v94
	v_fmamk_f32 v94, v35, 0xbc000000, v71
	v_fmac_f32_e32 v95, v94, v94
	v_fmamk_f32 v94, v35, 0xbc000000, v54
	v_fmac_f32_e32 v95, v94, v94
	v_fmamk_f32 v94, v35, 0xbc000000, v55
	v_fmac_f32_e32 v95, v94, v94
	v_fmamk_f32 v94, v35, 0xbc000000, v52
	v_fmac_f32_e32 v95, v94, v94
	v_fmamk_f32 v94, v35, 0xbc000000, v53
	v_fmac_f32_e32 v95, v94, v94
	v_fmamk_f32 v94, v35, 0xbc000000, v50
	v_fmac_f32_e32 v95, v94, v94
	v_fmamk_f32 v94, v35, 0xbc000000, v51
	v_fmac_f32_e32 v95, v94, v94
	v_fmamk_f32 v94, v35, 0xbc000000, v48
	v_fmac_f32_e32 v95, v94, v94
	v_fmamk_f32 v94, v35, 0xbc000000, v49
	v_fmac_f32_e32 v95, v94, v94
	v_fmamk_f32 v94, v35, 0xbc000000, v46
	v_fmac_f32_e32 v95, v94, v94
	v_fmamk_f32 v94, v35, 0xbc000000, v47
	v_fmac_f32_e32 v95, v94, v94
	v_fmamk_f32 v94, v35, 0xbc000000, v42
	v_fmac_f32_e32 v95, v94, v94
	v_fmamk_f32 v94, v35, 0xbc000000, v43
	v_mul_f32_e32 v34, 0x3c000000, v35
	v_fmac_f32_e32 v95, v94, v94
	v_fmamk_f32 v94, v35, 0xbc000000, v44
	v_fmamk_f32 v35, v35, 0xbc000000, v45
	v_fmac_f32_e32 v95, v94, v94
	v_pk_add_f32 v[138:139], v[88:89], v[34:35] op_sel_hi:[1,0] neg_lo:[0,1] neg_hi:[0,1]
	v_fmac_f32_e32 v95, v35, v35
	v_pk_mul_f32 v[88:89], v[138:139], v[138:139]
	s_nop 0
	v_add_f32_e32 v35, v88, v95
	v_add_f32_e32 v35, v89, v35
	v_pk_add_f32 v[40:41], v[40:41], v[34:35] op_sel_hi:[1,0] neg_lo:[0,1] neg_hi:[0,1]
	s_nop 0
	v_pk_mul_f32 v[88:89], v[40:41], v[40:41]
	s_nop 0
	v_add_f32_e32 v35, v88, v35
	v_add_f32_e32 v35, v89, v35
	v_pk_add_f32 v[140:141], v[90:91], v[34:35] op_sel_hi:[1,0] neg_lo:[0,1] neg_hi:[0,1]
	s_nop 0
	v_pk_mul_f32 v[88:89], v[140:141], v[140:141]
	s_nop 0
	v_add_f32_e32 v35, v88, v35
	v_add_f32_e32 v35, v89, v35
	v_pk_add_f32 v[142:143], v[92:93], v[34:35] op_sel_hi:[1,0] neg_lo:[0,1] neg_hi:[0,1]
	ds_read_b128 v[92:95], v150 offset:19648
	v_pk_mul_f32 v[88:89], v[142:143], v[142:143]
	s_nop 0
	v_add_f32_e32 v35, v88, v35
	v_add_f32_e32 v35, v89, v35
	ds_bpermute_b32 v104, v149, v35
	ds_read_b128 v[88:91], v150 offset:19584
	s_waitcnt lgkmcnt(1)
	v_add_f32_e32 v35, v35, v104
	ds_bpermute_b32 v104, v148, v35
	s_waitcnt lgkmcnt(0)
	v_add_f32_e32 v35, v35, v104
	v_fmac_f32_e32 v106, 0x3c000000, v35
	v_mul_f32_e32 v35, 0x4b800000, v106
	v_cmp_gt_f32_e32 vcc, s1, v106
	s_nop 1
	v_cndmask_b32_e32 v35, v106, v35, vcc
	v_rsq_f32_e32 v35, v35
	ds_read_b128 v[104:107], v150 offset:19840
	v_mul_f32_e32 v132, 0x45800000, v35
	v_cndmask_b32_e32 v132, v35, v132, vcc
	v_pk_add_f32 v[78:79], v[78:79], v[34:35] op_sel_hi:[1,0] neg_lo:[0,1] neg_hi:[0,1]
	v_cmp_lt_i32_e32 vcc, -1, v68
	v_pk_mul_f32 v[78:79], v[132:133], v[78:79] op_sel_hi:[0,1]
	v_pk_fma_f32 v[36:37], v[36:37], v[78:79], v[62:63]
	v_pk_add_f32 v[62:63], v[76:77], v[34:35] op_sel_hi:[1,0] neg_lo:[0,1] neg_hi:[0,1]
	s_nop 0
	v_pk_mul_f32 v[62:63], v[132:133], v[62:63] op_sel_hi:[0,1]
	v_pk_fma_f32 v[38:39], v[38:39], v[62:63], v[64:65]
	ds_write_b128 v57, v[36:39]
	v_pk_add_f32 v[36:37], v[74:75], v[34:35] op_sel_hi:[1,0] neg_lo:[0,1] neg_hi:[0,1]
	v_pk_add_f32 v[38:39], v[72:73], v[34:35] op_sel_hi:[1,0] neg_lo:[0,1] neg_hi:[0,1]
	v_pk_mul_f32 v[36:37], v[132:133], v[36:37] op_sel_hi:[0,1]
	v_pk_mul_f32 v[38:39], v[132:133], v[38:39] op_sel_hi:[0,1]
	v_pk_fma_f32 v[36:37], v[58:59], v[36:37], v[84:85]
	v_pk_fma_f32 v[38:39], v[60:61], v[38:39], v[86:87]
	ds_write_b128 v57, v[36:39] offset:64
	v_pk_add_f32 v[36:37], v[70:71], v[34:35] op_sel_hi:[1,0] neg_lo:[0,1] neg_hi:[0,1]
	v_pk_add_f32 v[38:39], v[54:55], v[34:35] op_sel_hi:[1,0] neg_lo:[0,1] neg_hi:[0,1]
	v_pk_mul_f32 v[36:37], v[132:133], v[36:37] op_sel_hi:[0,1]
	v_pk_mul_f32 v[38:39], v[132:133], v[38:39] op_sel_hi:[0,1]
	v_pk_fma_f32 v[36:37], v[88:89], v[36:37], v[96:97]
	v_pk_fma_f32 v[38:39], v[90:91], v[38:39], v[98:99]
	ds_write_b128 v57, v[36:39] offset:128
	v_pk_add_f32 v[36:37], v[52:53], v[34:35] op_sel_hi:[1,0] neg_lo:[0,1] neg_hi:[0,1]
	v_pk_add_f32 v[38:39], v[50:51], v[34:35] op_sel_hi:[1,0] neg_lo:[0,1] neg_hi:[0,1]
	v_pk_mul_f32 v[36:37], v[132:133], v[36:37] op_sel_hi:[0,1]
	v_pk_mul_f32 v[38:39], v[132:133], v[38:39] op_sel_hi:[0,1]
	v_pk_fma_f32 v[36:37], v[92:93], v[36:37], v[100:101]
	v_pk_fma_f32 v[38:39], v[94:95], v[38:39], v[102:103]
	ds_write_b128 v57, v[36:39] offset:192
	v_pk_add_f32 v[36:37], v[48:49], v[34:35] op_sel_hi:[1,0] neg_lo:[0,1] neg_hi:[0,1]
	v_pk_add_f32 v[38:39], v[46:47], v[34:35] op_sel_hi:[1,0] neg_lo:[0,1] neg_hi:[0,1]
	v_pk_mul_f32 v[36:37], v[132:133], v[36:37] op_sel_hi:[0,1]
	v_pk_mul_f32 v[38:39], v[132:133], v[38:39] op_sel_hi:[0,1]
	v_pk_fma_f32 v[36:37], v[108:109], v[36:37], v[116:117]
	v_pk_fma_f32 v[38:39], v[110:111], v[38:39], v[118:119]
	ds_write_b128 v57, v[36:39] offset:256
	v_pk_add_f32 v[36:37], v[42:43], v[34:35] op_sel_hi:[1,0] neg_lo:[0,1] neg_hi:[0,1]
	v_pk_add_f32 v[34:35], v[44:45], v[34:35] op_sel_hi:[1,0] neg_lo:[0,1] neg_hi:[0,1]
	v_pk_mul_f32 v[36:37], v[132:133], v[36:37] op_sel_hi:[0,1]
	v_pk_mul_f32 v[34:35], v[132:133], v[34:35] op_sel_hi:[0,1]
	v_pk_fma_f32 v[36:37], v[112:113], v[36:37], v[120:121]
	v_pk_fma_f32 v[38:39], v[114:115], v[34:35], v[122:123]
	ds_write_b128 v57, v[36:39] offset:320
	v_pk_mul_f32 v[34:35], v[132:133], v[138:139] op_sel_hi:[0,1]
	v_pk_mul_f32 v[36:37], v[132:133], v[40:41] op_sel_hi:[0,1]
	s_waitcnt lgkmcnt(6)
	v_pk_fma_f32 v[34:35], v[104:105], v[34:35], v[128:129]
	v_pk_fma_f32 v[36:37], v[106:107], v[36:37], v[130:131]
	ds_write_b128 v57, v[34:37] offset:384
	v_pk_mul_f32 v[34:35], v[132:133], v[140:141] op_sel_hi:[0,1]
	v_pk_mul_f32 v[36:37], v[132:133], v[142:143] op_sel_hi:[0,1]
	v_pk_fma_f32 v[34:35], v[124:125], v[34:35], v[134:135]
	v_pk_fma_f32 v[36:37], v[126:127], v[36:37], v[136:137]
	v_add_u32_e32 v50, v83, v69
	ds_write_b128 v57, v[34:37] offset:448
	ds_read_b32 v84, v56 offset:8
	ds_read_b32 v85, v56 offset:16
	ds_read_b32 v86, v56 offset:24
	ds_read_b32 v87, v56 offset:32
	ds_read_b32 v88, v56 offset:40
	ds_read_b32 v89, v56 offset:48
	ds_read_b32 v90, v56 offset:56
	ds_read_b128 v[100:103], v50
	ds_read_b128 v[104:107], v81
	ds_read_b128 v[108:111], v80
	ds_read_b128 v[112:115], v80 offset:1088
	ds_read_b128 v[116:119], v80 offset:2176
	ds_read_b128 v[120:123], v80 offset:3264
	ds_read_b128 v[124:127], v80 offset:4352
	ds_read_b128 v[128:131], v80 offset:5440
	v_or_b32_e32 v51, 0x4400, v150
	s_mov_b32 s1, s0
	v_mov_b32_e32 v97, 0
	v_cmp_lt_i32_e32 vcc, -1, v68
	v_lshlrev_b32_e32 v96, 9, v68
	v_lshl_add_u64 v[92:93], v[0:1], 0, v[96:97]
	s_waitcnt lgkmcnt(7)
	s_and_saveexec_b64 s[2:3], vcc
	global_store_dwordx4 v[92:93], v[100:103], off nt
	s_mov_b64 exec, s[2:3]
	v_cmp_lt_i32_e32 vcc, -1, v84
	v_lshlrev_b32_e32 v96, 9, v84
	v_lshl_add_u64 v[94:95], v[0:1], 0, v[96:97]
	s_waitcnt lgkmcnt(6)
	s_and_saveexec_b64 s[2:3], vcc
	global_store_dwordx4 v[94:95], v[104:107], off nt
	s_mov_b64 exec, s[2:3]
	v_cmp_lt_i32_e32 vcc, -1, v85
	v_lshlrev_b32_e32 v96, 9, v85
	v_lshl_add_u64 v[92:93], v[0:1], 0, v[96:97]
	s_waitcnt lgkmcnt(5)
	s_and_saveexec_b64 s[2:3], vcc
	global_store_dwordx4 v[92:93], v[108:111], off nt
	s_mov_b64 exec, s[2:3]
	v_cmp_lt_i32_e32 vcc, -1, v86
	v_lshlrev_b32_e32 v96, 9, v86
	v_lshl_add_u64 v[94:95], v[0:1], 0, v[96:97]
	s_waitcnt lgkmcnt(4)
	s_and_saveexec_b64 s[2:3], vcc
	global_store_dwordx4 v[94:95], v[112:115], off nt
	s_mov_b64 exec, s[2:3]
	v_cmp_lt_i32_e32 vcc, -1, v87
	v_lshlrev_b32_e32 v96, 9, v87
	v_lshl_add_u64 v[92:93], v[0:1], 0, v[96:97]
	s_waitcnt lgkmcnt(3)
	s_and_saveexec_b64 s[2:3], vcc
	global_store_dwordx4 v[92:93], v[116:119], off nt
	s_mov_b64 exec, s[2:3]
	v_cmp_lt_i32_e32 vcc, -1, v88
	v_lshlrev_b32_e32 v96, 9, v88
	v_lshl_add_u64 v[94:95], v[0:1], 0, v[96:97]
	s_waitcnt lgkmcnt(2)
	s_and_saveexec_b64 s[2:3], vcc
	global_store_dwordx4 v[94:95], v[120:123], off nt
	s_mov_b64 exec, s[2:3]
	v_cmp_lt_i32_e32 vcc, -1, v89
	v_lshlrev_b32_e32 v96, 9, v89
	v_lshl_add_u64 v[92:93], v[0:1], 0, v[96:97]
	s_waitcnt lgkmcnt(1)
	s_and_saveexec_b64 s[2:3], vcc
	global_store_dwordx4 v[92:93], v[124:127], off nt
	s_mov_b64 exec, s[2:3]
	v_cmp_lt_i32_e32 vcc, -1, v90
	v_lshlrev_b32_e32 v96, 9, v90
	v_lshl_add_u64 v[94:95], v[0:1], 0, v[96:97]
	s_waitcnt lgkmcnt(0)
	s_and_saveexec_b64 s[2:3], vcc
	global_store_dwordx4 v[94:95], v[128:131], off nt
	s_mov_b64 exec, s[2:3]
